# baseline (speedup 1.0000x reference)
_Z6k_attnILi1024ELi2048ELi1024ELi1024ELi2048ELi1024ELb1ELb1EEvPKDF16_S1_S1_PKfPDF16_:
	s_load_dwordx8 s[8:15], s[0:1], 0x0
	s_load_dwordx2 s[16:17], s[0:1], 0x20
	s_lshl_b32 s0, s2, 1
	s_and_b32 s20, s0, 14
	s_lshr_b32 s0, s2, 7
	s_add_i32 s20, s20, s0
	v_readfirstlane_b32 s42, v0
	s_lshr_b32 s0, s20, 2
	s_lshr_b32 s33, s42, 6
	s_mov_b32 s1, 0
	s_lshl_b32 s3, s2, 3
	s_lshr_b32 s4, s42, 2
	s_lshr_b32 s55, s2, 3
	s_and_b32 s55, s55, 7
	s_lshl_b32 s55, s55, 1
	s_lshr_b32 s6, s33, 2
	s_add_i32 s6, s6, s55
	s_lshl_b32 s6, s6, 6
	s_lshr_b32 s57, s33, 2
	s_lshl_b32 s57, s57, 12
	s_lshr_b32 s61, s33, 2
	s_mul_i32 s61, s61, 0x6800
	s_mov_b64 s[58:59], 0x80
	s_lshl_b64 s[22:23], s[0:1], 21
	s_and_b32 s3, s4, 48
	s_lshl_b32 s36, s33, 10
	s_cmp_lg_u32 0, -1
	s_cselect_b32 s5, 0, 0
	s_add_i32 s39, s36, s5
	s_waitcnt lgkmcnt(0)
	s_add_u32 s5, s10, s22
	v_bfe_u32 v202, v0, 2, 4
	s_addc_u32 s19, s11, s23
	v_or_b32_e32 v2, s3, v202
	s_add_u32 s18, s5, s6
	v_bfe_u32 v28, v0, 4, 2
	v_mov_b32_e32 v19, 0
	s_addc_u32 s19, s19, 0
	v_lshlrev_b32_e32 v18, 10, v2
	v_bitop3_b32 v1, v28, v0, 3 bitop3:0x78
	v_lshl_add_u64 v[4:5], s[18:19], 0, v[18:19]
	v_lshlrev_b32_e32 v18, 4, v1
	s_cmpk_lt_u32 s42, 0x100
	s_mov_b32 s7, s1
	v_and_b32_e32 v22, 3, v0
	s_cselect_b64 s[18:19], -1, 0
	s_cmpk_gt_u32 s42, 0xff
	v_lshl_add_u64 v[20:21], v[4:5], 0, v[18:19]
	s_nop 0
	s_mov_b32 m0, s39
	s_nop 0
	global_load_lds_dwordx4 v[20:21], off
.LBB6_2:
	s_lshl_b64 s[24:25], s[0:1], 23
	s_add_u32 s5, s12, s24
	s_addc_u32 s21, s13, s25
	s_lshl_b32 s26, s55, 7
	s_add_u32 s26, s5, s26
	s_addc_u32 s27, s21, 0
	v_lshlrev_b32_e32 v2, 12, v2
	v_mov_b32_e32 v3, v19
	v_lshl_add_u64 v[2:3], s[26:27], 0, v[2:3]
	s_and_b32 s26, s4, 0x3fffffc0
	s_cmp_lg_u32 0, -1
	s_mov_b32 s27, s1
	s_cselect_b32 s4, 0, 0
	v_lshl_add_u64 v[2:3], v[2:3], 0, s[26:27]
	v_lshlrev_b32_e32 v160, 4, v22
	v_mov_b32_e32 v161, v19
	s_add_i32 s4, s4, s36
	v_lshl_add_u64 v[162:163], v[2:3], 0, v[160:161]
	s_add_i32 s37, s4, 0x6000
	v_cndmask_b32_e64 v2, 0, 1, s[18:19]
	s_andn2_b64 vcc, exec, s[18:19]
	s_mov_b32 m0, s37
	s_nop 0
	global_load_lds_dwordx4 v[162:163], off
	v_lshl_add_u64 v[226:227], v[162:163], 0, s[58:59]
	s_add_i32 m0, s37, 0x6800
	s_nop 0
	global_load_lds_dwordx4 v[226:227], off
	v_and_b32_e32 v1, 63, v0
	v_cmp_ne_u32_e64 s[4:5], 1, v2
	s_nop 0
	s_mov_b64 s[18:19], 0x10000
	s_cmp_lg_u32 0, -1
	v_lshl_add_u64 v[2:3], v[20:21], 0, s[18:19]
	s_cselect_b32 s18, 0, 0
	s_add_i32 s18, s18, s36
	s_addk_i32 s18, 0x2000
	s_mov_b32 m0, s18
	s_nop 0
	global_load_lds_dwordx4 v[2:3], off
.LBB6_4:
	s_lshl_b32 s18, s20, 8
	s_and_b32 s18, s18, 0x300
	s_lshl_b64 s[0:1], s[0:1], 10
	s_or_b32 s0, s0, s18
	s_lshr_b32 s56, s2, 6
	s_and_b32 s56, s56, 1
	s_lshl_b32 s56, s56, 2
	s_and_b32 s18, s33, 3
	s_or_b32 s18, s18, s56
	s_lshl_b32 s18, s18, 5
	s_add_u32 s18, s0, s18
	v_and_b32_e32 v203, 31, v0
	s_addc_u32 s19, s1, 0
	v_or_b32_e32 v2, s18, v203
	v_mov_b32_e32 v3, s19
	v_lshrrev_b32_e32 v204, 5, v1
	v_lshlrev_b64 v[4:5], 13, v[2:3]
	v_lshlrev_b64 v[2:3], 10, v[2:3]
	v_lshl_add_u64 v[4:5], s[14:15], 0, v[4:5]
	v_lshlrev_b32_e32 v26, 4, v204
	v_mov_b32_e32 v27, 0
	v_lshl_add_u64 v[2:3], s[8:9], 0, v[2:3]
	v_lshl_add_u64 v[24:25], v[4:5], 0, v[26:27]
	v_lshl_add_u64 v[2:3], v[2:3], 0, s[6:7]
	v_and_b32_e32 v26, 32, v0
	v_lshl_add_u64 v[30:31], v[2:3], 0, v[26:27]
	global_load_dwordx4 v[100:103], v[30:31], off offset:16
	global_load_dwordx4 v[96:99], v[30:31], off
	s_and_b64 vcc, exec, s[4:5]
	s_nop 0
	s_mov_b64 s[0:1], 0x20000
	s_cmp_lg_u32 0, -1
	v_lshl_add_u64 v[24:25], v[20:21], 0, s[0:1]
	s_cselect_b32 s0, 0, 0
	s_add_i32 s0, s0, s36
	s_addk_i32 s0, 0x4000
	s_mov_b32 m0, s0
	s_nop 0
	global_load_lds_dwordx4 v[24:25], off
.LBB6_6:
	v_lshlrev_b32_e32 v30, 3, v22
	v_or_b32_e32 v22, s18, v28
	v_mov_b32_e32 v23, s19
	v_lshlrev_b64 v[22:23], 13, v[22:23]
	v_lshl_add_u64 v[80:81], s[14:15], 0, v[22:23]
	v_lshrrev_b32_e32 v104, 2, v203
	v_lshlrev_b32_e32 v22, 1, v204
	v_bfe_u32 v23, v203, 2, 2
	s_and_b32 s7, s33, 3
	s_lshl_b32 s7, s7, 13
	s_lshr_b32 s62, s33, 2
	s_lshl_b32 s62, s62, 17
	s_mov_b32 s63, 0
	s_lshr_b32 s64, s33, 2
	s_lshl_b32 s64, s64, 12
	s_add_i32 s65, s64, 0x8000
	v_bitop3_b32 v24, v22, v104, 3 bitop3:0x78
	v_bitop3_b32 v22, v22, v23, 1 bitop3:0x36
	s_cmp_lg_u32 0, -1
	v_lshlrev_b32_e32 v218, 4, v22
	v_bitop3_b32 v22, v28, v0, 15 bitop3:0x78
	s_cselect_b32 s0, 0, 0
	v_lshlrev_b32_e32 v26, 4, v22
	s_add_i32 s41, s0, s7
	v_lshl_add_u64 v[164:165], v[80:81], 0, v[26:27]
	s_mov_b64 s[0:1], 0x0
	v_and_b32_e32 v31, 15, v0
	v_lshl_add_u64 v[22:23], v[164:165], 0, s[0:1]
	v_lshl_add_u64 v[22:23], v[22:23], 0, s[62:63]
	s_add_i32 s38, s41, 0x14800
	s_add_i32 m0, s38, s64
	s_nop 0
	global_load_lds_dwordx4 v[22:23], off nt
	v_bitop3_b32 v22, v28, v31, 4 bitop3:0x36
	v_lshlrev_b32_e32 v26, 4, v22
	v_lshl_add_u64 v[22:23], v[80:81], 0, v[26:27]
	s_mov_b64 s[8:9], 0x8000
	v_lshlrev_b32_e32 v217, 4, v24
	v_lshl_add_u64 v[24:25], v[22:23], 0, s[8:9]
	v_lshl_add_u64 v[24:25], v[24:25], 0, s[62:63]
	s_add_i32 s8, s41, 0x14c00
	s_add_i32 m0, s8, s64
	s_nop 0
	global_load_lds_dwordx4 v[24:25], off nt
	v_bitop3_b32 v24, v28, v31, 8 bitop3:0x36
	v_lshlrev_b32_e32 v26, 4, v24
	v_lshl_add_u64 v[24:25], v[80:81], 0, v[26:27]
	s_mov_b64 s[8:9], 0x10000
	v_bitop3_b32 v26, v28, v31, 12 bitop3:0x36
	v_lshl_add_u64 v[82:83], v[24:25], 0, s[8:9]
	v_lshl_add_u64 v[82:83], v[82:83], 0, s[62:63]
	s_add_i32 s8, s41, 0x15000
	s_add_i32 m0, s8, s64
	s_nop 0
	global_load_lds_dwordx4 v[82:83], off nt
	v_lshlrev_b32_e32 v26, 4, v26
	v_lshl_add_u64 v[26:27], v[80:81], 0, v[26:27]
	s_mov_b64 s[8:9], 0x18000
	v_lshl_add_u64 v[80:81], v[26:27], 0, s[8:9]
	v_lshl_add_u64 v[80:81], v[80:81], 0, s[62:63]
	s_add_i32 s8, s41, 0x15400
	s_add_i32 m0, s8, s64
	s_nop 0
	global_load_lds_dwordx4 v[80:81], off nt
	s_mov_b64 s[14:15], 0x20000
	s_add_i32 s14, s41, 0x15800
	s_mov_b64 s[14:15], 0x28000
	s_add_i32 s14, s41, 0x15c00
	s_mov_b64 s[34:35], 0x30000
	s_add_i32 s34, s41, 0x16000
	s_mov_b64 s[34:35], 0x38000
	v_lshl_add_u32 v216, v203, 6, 0
	v_add_u32_e32 v216, s57, v216
	s_add_i32 s41, s41, 0x16400
	s_waitcnt vmcnt(0) lgkmcnt(0)
	s_barrier
	v_and_b32_e32 v226, 31, v0
	v_bfe_u32 v227, v0, 5, 1
	v_lshrrev_b32_e32 v228, 2, v226
	v_lshlrev_b32_e32 v228, 10, v228
	v_and_b32_e32 v229, 3, v226
	v_lshlrev_b32_e32 v229, 8, v229
	v_add3_u32 v230, s38, v228, v229
	v_and_b32_e32 v231, 15, v226
	v_xor_b32_e32 v231, v231, v227
	v_lshlrev_b32_e32 v231, 4, v231
	v_mov_b32_e32 v232, v231
	v_add_u32_e32 v232, v230, v232
	ds_read_b128 v[64:67], v232
	v_xor_b32_e32 v233, 0x80, v231
	v_add_u32_e32 v233, v230, v233
	ds_read_b128 v[2:5], v233
	v_xor_b32_e32 v234, 0x20, v231
	v_add_u32_e32 v234, v230, v234
	ds_read_b128 v[68:71], v234
	v_xor_b32_e32 v235, 0xa0, v231
	v_add_u32_e32 v235, v230, v235
	ds_read_b128 v[6:9], v235
	v_xor_b32_e32 v236, 0x40, v231
	v_add_u32_e32 v236, v230, v236
	ds_read_b128 v[72:75], v236
	v_xor_b32_e32 v237, 0xc0, v231
	v_add_u32_e32 v237, v230, v237
	ds_read_b128 v[10:13], v237
	v_xor_b32_e32 v238, 0x60, v231
	v_add_u32_e32 v238, v230, v238
	ds_read_b128 v[76:79], v238
	v_xor_b32_e32 v239, 0xe0, v231
	v_add_u32_e32 v239, v230, v239
	ds_read_b128 v[14:17], v239
	s_waitcnt lgkmcnt(0)
	s_mov_b64 s[52:53], 0x100
	v_lshl_add_u64 v[224:225], v[164:165], 0, s[52:53]
	v_lshl_add_u64 v[224:225], v[224:225], 0, s[62:63]
	s_add_i32 s54, s38, 0x0
	s_add_i32 m0, s54, s65
	s_nop 0
	global_load_lds_dwordx4 v[224:225], off nt
	s_mov_b64 s[52:53], 0x8100
	v_lshl_add_u64 v[224:225], v[22:23], 0, s[52:53]
	v_lshl_add_u64 v[224:225], v[224:225], 0, s[62:63]
	s_add_i32 s54, s38, 0x400
	s_add_i32 m0, s54, s65
	s_nop 0
	global_load_lds_dwordx4 v[224:225], off nt
	s_mov_b64 s[52:53], 0x10100
	v_lshl_add_u64 v[224:225], v[24:25], 0, s[52:53]
	v_lshl_add_u64 v[224:225], v[224:225], 0, s[62:63]
	s_add_i32 s54, s38, 0x800
	s_add_i32 m0, s54, s65
	s_nop 0
	global_load_lds_dwordx4 v[224:225], off nt
	s_mov_b64 s[52:53], 0x18100
	v_lshl_add_u64 v[224:225], v[26:27], 0, s[52:53]
	v_lshl_add_u64 v[224:225], v[224:225], 0, s[62:63]
	s_add_i32 s54, s38, 0xc00
	s_add_i32 m0, s54, s65
	s_nop 0
	global_load_lds_dwordx4 v[224:225], off nt
	s_mov_b64 s[52:53], 0x20100
	s_add_i32 s54, s38, 0x1000
	s_mov_b64 s[52:53], 0x28100
	s_add_i32 s54, s38, 0x1400
	s_mov_b64 s[52:53], 0x30100
	s_add_i32 s54, s38, 0x1800
	s_mov_b64 s[52:53], 0x38100
	s_add_i32 s54, s38, 0x1c00
	v_add_u32_e32 v209, v216, v217
	v_add_u32_e32 v210, v216, v218
	ds_read_b128 v[80:83], v209
	ds_read_b128 v[88:91], v209 offset:2048
	ds_read_b128 v[84:87], v210
	ds_read_b128 v[92:95], v210 offset:2048
	v_mov_b32_e32 v219, 0x7f7f7f7f
	v_mov_b32_e32 v220, 0x7c7c7c7c
	s_waitcnt vmcnt(10) lgkmcnt(1)
	v_mfma_scale_f32_32x32x64_f8f6f4 v[64:79], v[80:87], v[96:103], v[64:79], v219, v220 op_sel_hi:[0,0,0]
	s_waitcnt vmcnt(8) lgkmcnt(0)
	v_mfma_scale_f32_32x32x64_f8f6f4 v[2:17], v[88:95], v[96:103], v[2:17], v219, v220 op_sel_hi:[0,0,0]
	s_mov_b32 s41, 0x3fb8aa3b
	s_nop 15
	s_nop 15
	s_nop 15
	s_nop 15
	s_nop 15
	s_nop 15
	s_waitcnt vmcnt(0) lgkmcnt(0)
	s_barrier
	v_lshlrev_b32_e32 v29, 2, v204
	v_max_f32_e32 v80, v65, v65
	v_max_f32_e32 v81, v64, v64
	v_max_f32_e32 v80, v81, v80
	v_max3_f32 v81, v66, v67, v3
	v_max3_f32 v80, v80, v2, v4
	v_max3_f32 v80, v80, v5, v68
	v_max3_f32 v81, v81, v70, v71
	v_max3_f32 v80, v80, v69, v6
	v_max3_f32 v81, v81, v8, v9
	v_max3_f32 v80, v80, v7, v72
	v_max3_f32 v81, v81, v74, v75
	v_max3_f32 v80, v80, v73, v10
	v_max3_f32 v81, v81, v12, v13
	v_max3_f32 v80, v80, v11, v76
	v_max3_f32 v81, v81, v78, v79
	v_max3_f32 v80, v80, v77, v14
	v_max3_f32 v81, v81, v16, v17
	v_max3_f32 v80, v80, v15, v81
	v_mov_b32_e32 v81, v80
	s_nop 1
	v_permlane32_swap_b32_e32 v80, v81
	v_max_f32_e32 v81, v81, v81
	v_max_f32_e32 v80, v80, v80
	v_max_f32_e32 v80, v80, v81
	v_mul_f32_e32 v208, 0x3fb8aa3b, v80
	s_mov_b32 s27, 0
	s_mov_b32 s40, -1
	s_mov_b64 s[0:1], 0x8000
	s_mov_b64 s[28:29], 0x10000
	s_mov_b64 s[20:21], 0x18000
	s_mov_b64 s[8:9], 0x20000
	s_mov_b64 s[30:31], 0x28000
	s_mov_b64 s[14:15], 0x30000
	s_mov_b64 s[34:35], 0x38000
	v_fma_f32 v64, v64, s41, -v208
	v_fma_f32 v2, v2, s41, -v208
	v_fma_f32 v65, v65, s41, -v208
	v_fma_f32 v3, v3, s41, -v208
	v_fma_f32 v66, v66, s41, -v208
	v_fma_f32 v4, v4, s41, -v208
	v_fma_f32 v67, v67, s41, -v208
	v_fma_f32 v5, v5, s41, -v208
	v_fma_f32 v68, v68, s41, -v208
	v_fma_f32 v6, v6, s41, -v208
	v_fma_f32 v69, v69, s41, -v208
	v_fma_f32 v7, v7, s41, -v208
	v_fma_f32 v70, v70, s41, -v208
	v_fma_f32 v8, v8, s41, -v208
	v_fma_f32 v71, v71, s41, -v208
	v_fma_f32 v9, v9, s41, -v208
	v_fma_f32 v72, v72, s41, -v208
	v_fma_f32 v10, v10, s41, -v208
	v_fma_f32 v73, v73, s41, -v208
	v_fma_f32 v11, v11, s41, -v208
	v_fma_f32 v74, v74, s41, -v208
	v_fma_f32 v12, v12, s41, -v208
	v_fma_f32 v75, v75, s41, -v208
	v_fma_f32 v13, v13, s41, -v208
	v_fma_f32 v76, v76, s41, -v208
	v_fma_f32 v14, v14, s41, -v208
	v_fma_f32 v77, v77, s41, -v208
	v_fma_f32 v78, v78, s41, -v208
	v_fma_f32 v79, v79, s41, -v208
	v_fma_f32 v94, v15, s41, -v208
	v_fma_f32 v16, v16, s41, -v208
	v_fma_f32 v15, v17, s41, -v208
	s_and_b64 vcc, exec, s[4:5]
	s_nop 0
	v_lshl_add_u64 v[20:21], v[20:21], 0, s[14:15]
	s_mov_b32 m0, s39
	s_nop 0
	global_load_lds_dwordx4 v[20:21], off
.LBB6_8:
	v_lshl_add_u64 v[178:179], v[22:23], 0, s[0:1]
	s_and_b32 s0, s42, 0x3fffffc0
	s_lshl_b32 s0, s0, 2
	s_add_i32 s45, s0, 0
	s_add_i32 s0, s7, 0
	s_add_i32 s0, s0, 0x14800
	v_lshlrev_b32_e32 v0, 8, v0
	s_cmp_lg_u32 0, -1
	v_lshl_add_u64 v[170:171], v[22:23], 0, s[30:31]
	v_exp_f32_e32 v80, v64
	v_exp_f32_e32 v64, v2
	v_lshlrev_b32_e32 v2, 10, v104
	v_and_b32_e32 v0, 0x300, v0
	s_cselect_b32 s30, 0, 0
	v_add3_u32 v222, s0, v2, v0
	s_add_i32 s0, s30, s36
	s_add_i32 s44, s30, s7
	v_lshl_add_u64 v[166:167], v[26:27], 0, s[34:35]
	s_add_i32 s0, s0, 0x8000
	s_add_i32 s30, s44, 0x14c00
	s_add_i32 s31, s44, 0x15000
	s_add_i32 s34, s44, 0x15400
	s_add_i32 s35, s44, 0x15800
	s_add_i32 s42, s44, 0x15c00
	s_add_i32 s43, s44, 0x16000
	s_add_i32 s44, s44, 0x16400
	v_lshlrev_b32_e32 v0, 5, v28
	v_lshrrev_b32_e32 v2, 2, v31
	s_add_u32 s22, s6, s22
	v_and_b32_e32 v0, 32, v0
	v_or_b32_e32 v2, v29, v2
	s_addc_u32 s23, 0, s23
	s_lshl_b32 s2, s55, 7
	v_lshl_add_u64 v[174:175], v[26:27], 0, s[20:21]
	v_exp_f32_e32 v87, v71
	v_exp_f32_e32 v71, v9
	v_add_u32_e32 v0, 0, v0
	v_lshlrev_b32_e32 v2, 6, v2
	s_mov_b64 s[20:21], 0x40000
	v_add_u32_e32 v9, s3, v202
	s_and_b32 s2, s2, 0x780
	v_exp_f32_e32 v81, v65
	v_exp_f32_e32 v65, v3
	v_add3_u32 v207, v0, v30, v2
	v_add_u32_e32 v207, s61, v207
	v_lshl_add_u64 v[2:3], v[162:163], 0, s[20:21]
	s_mov_b32 m0, s0
	s_nop 0
	global_load_lds_dwordx4 v[2:3], off
	v_lshl_add_u64 v[226:227], v[2:3], 0, s[58:59]
	s_add_i32 m0, s0, 0x6800
	s_nop 0
	global_load_lds_dwordx4 v[226:227], off
	v_lshlrev_b32_e32 v184, 10, v9
	v_mov_b32_e32 v185, 0
	s_add_u32 s2, s26, s2
	ds_read_b128 v[112:115], v209 offset:8192
	ds_read_b128 v[104:107], v209 offset:10240
	ds_read_b128 v[116:119], v210 offset:8192
	ds_read_b128 v[108:111], v210 offset:10240
	v_cmp_gt_u32_e64 s[0:1], 32, v1
	v_lshl_add_u64 v[0:1], s[22:23], 0, v[184:185]
	s_addc_u32 s3, 0, 0
	v_lshl_add_u64 v[0:1], v[0:1], 0, v[18:19]
	s_add_u32 s2, s2, s24
	v_lshl_add_u64 v[0:1], s[10:11], 0, v[0:1]
	v_lshlrev_b32_e32 v184, 12, v9
	s_addc_u32 s3, s3, s25
	v_exp_f32_e32 v82, v66
	v_exp_f32_e32 v66, v4
	v_exp_f32_e32 v83, v67
	v_exp_f32_e32 v67, v5
	v_exp_f32_e32 v84, v68
	v_exp_f32_e32 v68, v6
	v_exp_f32_e32 v85, v69
	v_exp_f32_e32 v69, v7
	v_exp_f32_e32 v86, v70
	v_exp_f32_e32 v70, v8
	v_exp_f32_e32 v88, v72
	v_exp_f32_e32 v72, v10
	v_exp_f32_e32 v89, v73
	v_exp_f32_e32 v73, v11
	v_exp_f32_e32 v90, v74
	v_exp_f32_e32 v74, v12
	v_exp_f32_e32 v91, v75
	v_exp_f32_e32 v75, v13
	v_exp_f32_e32 v92, v76
	v_exp_f32_e32 v76, v14
	v_exp_f32_e32 v93, v77
	v_exp_f32_e32 v77, v94
	v_exp_f32_e32 v94, v78
	v_exp_f32_e32 v78, v16
	v_exp_f32_e32 v95, v79
	v_exp_f32_e32 v79, v15
	v_xor_b32_e32 v4, v204, v31
	v_lshl_add_u64 v[180:181], v[0:1], 0, s[28:29]
	v_lshl_add_u64 v[0:1], s[2:3], 0, v[184:185]
	v_mov_b32_e32 v161, v185
	s_waitcnt vmcnt(3) lgkmcnt(0)
	s_barrier
	v_lshlrev_b32_e32 v223, 4, v4
	v_lshl_add_u64 v[0:1], v[0:1], 0, v[160:161]
	v_xor_b32_e32 v2, 0x80, v223
	v_xor_b32_e32 v3, 32, v223
	v_xor_b32_e32 v4, 0xa0, v223
	v_xor_b32_e32 v5, 64, v223
	v_xor_b32_e32 v6, 0xc0, v223
	v_xor_b32_e32 v7, 0x60, v223
	v_xor_b32_e32 v8, 0xe0, v223
	v_lshl_add_u64 v[0:1], s[12:13], 0, v[0:1]
	v_lshl_add_u64 v[176:177], v[24:25], 0, s[28:29]
	v_lshl_add_u64 v[172:173], v[164:165], 0, s[8:9]
	v_lshl_add_u64 v[168:169], v[24:25], 0, s[14:15]
	v_lshl_add_u32 v206, v203, 2, s45
	v_lshl_add_u32 v205, v29, 2, s45
	v_lshl_add_u64 v[182:183], v[0:1], 0, s[20:21]
	s_movk_i32 s28, 0x4000
	s_movk_i32 s45, 0x2000
	s_mov_b64 s[2:3], 0
	s_mov_b32 s29, 0x41000000
	s_mov_b64 s[10:11], 0x300
	s_mov_b64 s[12:13], 0x80000
	s_mov_b64 s[22:23], 0x400
	v_add_u32_e32 v161, v222, v2
	v_add_u32_e32 v184, v222, v3
	v_add_u32_e32 v211, v222, v4
	v_add_u32_e32 v212, v222, v5
	v_add_u32_e32 v213, v222, v6
	v_add_u32_e32 v214, v222, v7
	v_add_u32_e32 v215, v222, v8
	v_mov_b32_e32 v0, v185
	v_mov_b32_e32 v1, v185
	v_mov_b32_e32 v2, v185
	v_mov_b32_e32 v3, v185
	v_mov_b32_e32 v4, v185
	v_mov_b32_e32 v5, v185
	v_mov_b32_e32 v6, v185
	v_mov_b32_e32 v7, v185
	v_mov_b32_e32 v8, v185
	v_mov_b32_e32 v9, v185
	v_mov_b32_e32 v10, v185
	v_mov_b32_e32 v11, v185
	v_mov_b32_e32 v12, v185
	v_mov_b32_e32 v13, v185
	v_mov_b32_e32 v14, v185
	v_mov_b32_e32 v15, v185
	v_mov_b32_e32 v16, v185
	v_mov_b32_e32 v17, v185
	v_mov_b32_e32 v18, v185
	v_mov_b32_e32 v19, v185
	v_mov_b32_e32 v20, v185
	v_mov_b32_e32 v21, v185
	v_mov_b32_e32 v22, v185
	v_mov_b32_e32 v23, v185
	v_mov_b32_e32 v24, v185
	v_mov_b32_e32 v25, v185
	v_mov_b32_e32 v26, v185
	v_mov_b32_e32 v27, v185
	v_mov_b32_e32 v28, v185
	v_mov_b32_e32 v29, v185
	v_mov_b32_e32 v30, v185
	v_mov_b32_e32 v31, v185
	v_add_u32_e32 v221, v222, v223
	ds_read_b128 v[48:51], v221 offset:32768
	ds_read_b128 v[32:35], v161 offset:32768
	ds_read_b128 v[52:55], v184 offset:32768
	ds_read_b128 v[36:39], v211 offset:32768
	ds_read_b128 v[56:59], v212 offset:32768
	ds_read_b128 v[40:43], v213 offset:32768
	ds_read_b128 v[60:63], v214 offset:32768
	ds_read_b128 v[44:47], v215 offset:32768
	s_waitcnt lgkmcnt(0)
	s_mov_b64 s[52:53], 0x200
	v_lshl_add_u64 v[224:225], v[164:165], 0, s[52:53]
	v_lshl_add_u64 v[224:225], v[224:225], 0, s[62:63]
	s_add_i32 m0, s38, s64
	s_nop 0
	global_load_lds_dwordx4 v[224:225], off nt
	v_lshl_add_u64 v[224:225], v[178:179], 0, s[52:53]
	v_lshl_add_u64 v[224:225], v[224:225], 0, s[62:63]
	s_add_i32 m0, s30, s64
	s_nop 0
	global_load_lds_dwordx4 v[224:225], off nt
	v_lshl_add_u64 v[224:225], v[176:177], 0, s[52:53]
	v_lshl_add_u64 v[224:225], v[224:225], 0, s[62:63]
	s_add_i32 m0, s31, s64
	s_nop 0
	global_load_lds_dwordx4 v[224:225], off nt
	v_lshl_add_u64 v[224:225], v[174:175], 0, s[52:53]
	v_lshl_add_u64 v[224:225], v[224:225], 0, s[62:63]
	s_add_i32 m0, s34, s64
	s_nop 0
	global_load_lds_dwordx4 v[224:225], off nt
.LBB6_9:
	v_add_u32_e32 v138, s27, v207
	ds_read_b64_tr_b16 v[156:157], v138 offset:24576
	ds_read_b64_tr_b16 v[158:159], v138 offset:25088
	v_add_f32_e32 v120, v80, v81
	s_waitcnt lgkmcnt(3)
	v_mfma_scale_f32_32x32x64_f8f6f4 v[48:63], v[112:119], v[96:103], v[48:63], v219, v220 op_sel_hi:[0,0,0]
	v_add_f32_e32 v112, v82, v120
	v_add_f32_e32 v112, v83, v112
	v_add_f32_e32 v112, v84, v112
	v_add_f32_e32 v116, v85, v112
	v_cvt_pk_f16_f32 v132, v80, v81
	v_cvt_pk_f16_f32 v133, v82, v83
	ds_read_b64_tr_b16 v[112:113], v138 offset:28672
	ds_read_b64_tr_b16 v[114:115], v138 offset:29184
	v_add_f32_e32 v80, v86, v116
	v_add_f32_e32 v80, v87, v80
	v_add_f32_e32 v80, v88, v80
	v_add_f32_e32 v80, v89, v80
	v_cvt_pk_f16_f32 v134, v84, v85
	v_cvt_pk_f16_f32 v135, v86, v87
	s_waitcnt lgkmcnt(4)
	v_mfma_scale_f32_32x32x64_f8f6f4 v[32:47], v[104:111], v[96:103], v[32:47], v219, v220 op_sel_hi:[0,0,0]
	ds_read_b64_tr_b16 v[104:105], v138 offset:25600
	ds_read_b64_tr_b16 v[106:107], v138 offset:26112
	v_add_f32_e32 v80, v90, v80
	v_add_f32_e32 v80, v91, v80
	v_add_f32_e32 v80, v92, v80
	v_add_f32_e32 v80, v93, v80
	v_cvt_pk_f16_f32 v128, v88, v89
	v_cvt_pk_f16_f32 v129, v90, v91
	ds_read_b64_tr_b16 v[152:153], v138 offset:29696
	ds_read_b64_tr_b16 v[154:155], v138 offset:30208
	v_add_f32_e32 v80, v94, v80
	v_add_f32_e32 v80, v95, v80
	v_add_f32_e32 v80, v64, v80
	v_add_f32_e32 v80, v65, v80
	v_cvt_pk_f16_f32 v130, v92, v93
	v_cvt_pk_f16_f32 v131, v94, v95
	ds_read_b64_tr_b16 v[148:149], v138 offset:26624
	ds_read_b64_tr_b16 v[150:151], v138 offset:27136
	v_add_f32_e32 v80, v66, v80
	v_add_f32_e32 v80, v67, v80
	v_add_f32_e32 v80, v68, v80
	v_add_f32_e32 v80, v69, v80
	v_cvt_pk_f16_f32 v124, v64, v65
	v_cvt_pk_f16_f32 v125, v66, v67
	ds_read_b64_tr_b16 v[144:145], v138 offset:30720
	ds_read_b64_tr_b16 v[146:147], v138 offset:31232
	v_add_f32_e32 v64, v70, v80
	v_add_f32_e32 v64, v71, v64
	v_add_f32_e32 v64, v72, v64
	v_add_f32_e32 v64, v73, v64
	v_cvt_pk_f16_f32 v126, v68, v69
	v_cvt_pk_f16_f32 v127, v70, v71
	ds_read_b64_tr_b16 v[140:141], v138 offset:27648
	ds_read_b64_tr_b16 v[142:143], v138 offset:28160
	v_add_f32_e32 v64, v74, v64
	v_add_f32_e32 v64, v75, v64
	v_add_f32_e32 v64, v76, v64
	v_add_f32_e32 v64, v77, v64
	v_cvt_pk_f16_f32 v120, v72, v73
	v_cvt_pk_f16_f32 v121, v74, v75
	ds_read_b64_tr_b16 v[136:137], v138 offset:31744
	ds_read_b64_tr_b16 v[138:139], v138 offset:32256
	v_add_f32_e32 v64, v78, v64
	v_add_f32_e32 v64, v79, v64
	v_add_f32_e32 v108, 0, v64
	v_cvt_pk_f16_f32 v122, v76, v77
	v_cvt_pk_f16_f32 v123, v78, v79
	s_nop 1
	s_nop 0
	v_add_f32_e32 v185, v185, v108
	v_max_f32_e32 v108, v49, v49
	v_max_f32_e32 v109, v48, v48
	v_max_f32_e32 v108, v109, v108
	v_max3_f32 v109, v50, v51, v33
	v_max3_f32 v108, v108, v32, v34
	v_max3_f32 v108, v108, v35, v52
	v_max3_f32 v109, v109, v54, v55
	v_max3_f32 v108, v108, v53, v36
	v_max3_f32 v109, v109, v38, v39
	v_max3_f32 v108, v108, v37, v56
	v_max3_f32 v109, v109, v58, v59
	s_waitcnt vmcnt(0)
	s_barrier
	v_add_u32_e32 v221, v222, v223
	v_max3_f32 v108, v108, v57, v40
	v_max3_f32 v109, v109, v42, v43
	ds_read_b128 v[80:83], v221
	ds_read_b128 v[64:67], v161
	ds_read_b128 v[84:87], v184
	ds_read_b128 v[68:71], v211
	ds_read_b128 v[88:91], v212
	ds_read_b128 v[72:75], v213
	ds_read_b128 v[92:95], v214
	ds_read_b128 v[76:79], v215
	v_max3_f32 v108, v108, v41, v60
	v_max3_f32 v109, v109, v62, v63
	v_max3_f32 v108, v108, v61, v44
	v_max3_f32 v109, v109, v46, v47
	v_max3_f32 v108, v108, v45, v109
	v_mov_b32_e32 v109, v108
	s_nop 1
	v_permlane32_swap_b32_e32 v108, v109
	v_max_f32_e32 v109, v109, v109
	v_max_f32_e32 v108, v108, v108
	v_max_f32_e32 v108, v108, v109
	v_fma_f32 v108, v108, s41, -v208
	v_cmp_lt_f32_e32 vcc, s29, v108
	s_cmp_lg_u64 vcc, 0
	s_cselect_b64 s[24:25], -1, 0
	s_cbranch_vccnz .LBB6_21
.LBB6_10:
	s_waitcnt lgkmcnt(14)
	v_mfma_f32_32x32x16_f16 v[0:15], v[132:135], v[156:159], v[0:15]
	v_fma_f32 v48, v48, s41, -v208
	v_fma_f32 v49, v49, s41, -v208
	v_fma_f32 v50, v50, s41, -v208
	v_fma_f32 v51, v51, s41, -v208
	v_exp_f32_e32 v48, v48
	v_exp_f32_e32 v49, v49
	v_exp_f32_e32 v50, v50
	v_exp_f32_e32 v51, v51
	s_and_b64 vcc, exec, s[4:5]
	s_nop 0
	v_lshl_add_u64 v[108:109], v[180:181], 0, s[14:15]
	s_add_i32 s26, s45, s39
	s_mov_b32 m0, s26
	s_nop 0
	global_load_lds_dwordx4 v[108:109], off
.LBB6_12:
	v_mfma_f32_32x32x16_f16 v[16:31], v[132:135], v[112:115], v[16:31]
	v_fma_f32 v52, v52, s41, -v208
	v_fma_f32 v53, v53, s41, -v208
	v_fma_f32 v54, v54, s41, -v208
	v_fma_f32 v55, v55, s41, -v208
	v_exp_f32_e32 v52, v52
	v_exp_f32_e32 v53, v53
	v_exp_f32_e32 v54, v54
	v_exp_f32_e32 v55, v55
	v_lshl_add_u64 v[108:109], v[182:183], 0, s[20:21]
	s_add_i32 s26, s28, s37
	s_mov_b32 m0, s26
	s_nop 0
	global_load_lds_dwordx4 v[108:109], off
	v_lshl_add_u64 v[226:227], v[108:109], 0, s[58:59]
	s_add_i32 m0, s26, 0x6800
	s_nop 0
	global_load_lds_dwordx4 v[226:227], off
	s_waitcnt lgkmcnt(0)
	v_lshl_add_u64 v[186:187], v[164:165], 0, s[2:3]
	v_lshl_add_u64 v[108:109], v[186:187], 0, s[10:11]
	v_lshl_add_u64 v[108:109], v[108:109], 0, s[62:63]
	s_add_i32 m0, s38, s65
	s_nop 0
	global_load_lds_dwordx4 v[108:109], off nt
	v_add_u32_e32 v108, s28, v216
	v_add_u32_e32 v109, v108, v217
	v_add_u32_e32 v108, v108, v218
	ds_read_b128 v[112:115], v109
	ds_read_b128 v[116:119], v108
	v_mfma_f32_32x32x16_f16 v[0:15], v[128:131], v[104:107], v[0:15]
	v_fma_f32 v56, v56, s41, -v208
	v_fma_f32 v57, v57, s41, -v208
	v_fma_f32 v58, v58, s41, -v208
	v_fma_f32 v59, v59, s41, -v208
	v_exp_f32_e32 v56, v56
	v_exp_f32_e32 v57, v57
	v_exp_f32_e32 v58, v58
	v_exp_f32_e32 v59, v59
	v_lshl_add_u64 v[188:189], v[178:179], 0, s[2:3]
	v_lshl_add_u64 v[104:105], v[188:189], 0, s[10:11]
	v_lshl_add_u64 v[104:105], v[104:105], 0, s[62:63]
	s_add_i32 m0, s30, s65
	s_nop 0
	global_load_lds_dwordx4 v[104:105], off nt
	ds_read_b128 v[104:107], v109 offset:2048
	ds_read_b128 v[108:111], v108 offset:2048
	v_mfma_f32_32x32x16_f16 v[16:31], v[128:131], v[152:155], v[16:31]
	v_fma_f32 v60, v60, s41, -v208
	v_fma_f32 v61, v61, s41, -v208
	v_fma_f32 v62, v62, s41, -v208
	v_fma_f32 v63, v63, s41, -v208
	v_exp_f32_e32 v60, v60
	v_exp_f32_e32 v61, v61
	v_exp_f32_e32 v62, v62
	v_exp_f32_e32 v63, v63
	v_lshl_add_u64 v[190:191], v[176:177], 0, s[2:3]
	v_lshl_add_u64 v[128:129], v[190:191], 0, s[10:11]
	v_lshl_add_u64 v[128:129], v[128:129], 0, s[62:63]
	s_add_i32 m0, s31, s65
	s_nop 0
	global_load_lds_dwordx4 v[128:129], off nt
	v_mfma_f32_32x32x16_f16 v[0:15], v[124:127], v[148:151], v[0:15]
	v_fma_f32 v32, v32, s41, -v208
	v_fma_f32 v33, v33, s41, -v208
	v_fma_f32 v34, v34, s41, -v208
	v_fma_f32 v35, v35, s41, -v208
	v_exp_f32_e32 v32, v32
	v_exp_f32_e32 v33, v33
	v_exp_f32_e32 v34, v34
	v_exp_f32_e32 v35, v35
	v_lshl_add_u64 v[192:193], v[174:175], 0, s[2:3]
	v_lshl_add_u64 v[128:129], v[192:193], 0, s[10:11]
	v_lshl_add_u64 v[128:129], v[128:129], 0, s[62:63]
	s_add_i32 m0, s34, s65
	s_nop 0
	global_load_lds_dwordx4 v[128:129], off nt
	s_waitcnt lgkmcnt(14)
	v_mfma_f32_32x32x16_f16 v[16:31], v[124:127], v[144:147], v[16:31]
	v_fma_f32 v36, v36, s41, -v208
	v_fma_f32 v37, v37, s41, -v208
	v_fma_f32 v38, v38, s41, -v208
	v_fma_f32 v39, v39, s41, -v208
	v_exp_f32_e32 v36, v36
	v_exp_f32_e32 v37, v37
	v_exp_f32_e32 v38, v38
	v_exp_f32_e32 v39, v39
	v_lshl_add_u64 v[194:195], v[172:173], 0, s[2:3]
	v_mfma_f32_32x32x16_f16 v[0:15], v[120:123], v[140:143], v[0:15]
	v_fma_f32 v40, v40, s41, -v208
	v_fma_f32 v41, v41, s41, -v208
	v_fma_f32 v42, v42, s41, -v208
	v_fma_f32 v43, v43, s41, -v208
	v_exp_f32_e32 v40, v40
	v_exp_f32_e32 v41, v41
	v_exp_f32_e32 v42, v42
	v_exp_f32_e32 v43, v43
	v_lshl_add_u64 v[196:197], v[170:171], 0, s[2:3]
	s_waitcnt lgkmcnt(12)
	v_mfma_f32_32x32x16_f16 v[16:31], v[120:123], v[136:139], v[16:31]
	v_fma_f32 v44, v44, s41, -v208
	v_fma_f32 v45, v45, s41, -v208
	v_fma_f32 v46, v46, s41, -v208
	v_fma_f32 v47, v47, s41, -v208
	v_exp_f32_e32 v44, v44
	v_exp_f32_e32 v45, v45
	v_exp_f32_e32 v46, v46
	v_exp_f32_e32 v47, v47
	v_lshl_add_u64 v[198:199], v[168:169], 0, s[2:3]
	v_lshl_add_u64 v[200:201], v[166:167], 0, s[2:3]
	s_waitcnt vmcnt(7) lgkmcnt(0)
	s_barrier
	s_andn2_b64 vcc, exec, s[24:25]
	s_cbranch_vccnz .LBB6_14
	ds_read_b128 v[136:139], v205 offset:49248
	ds_read_b128 v[140:143], v205 offset:49216
	ds_read_b128 v[144:147], v205 offset:49184
	ds_read_b128 v[148:151], v205 offset:49152
	s_waitcnt lgkmcnt(3)
	v_pk_mul_f32 v[14:15], v[14:15], v[138:139]
	s_waitcnt lgkmcnt(2)
	v_pk_mul_f32 v[10:11], v[10:11], v[142:143]
	s_waitcnt lgkmcnt(1)
	v_pk_mul_f32 v[6:7], v[6:7], v[146:147]
	s_waitcnt lgkmcnt(0)
	v_pk_mul_f32 v[2:3], v[2:3], v[150:151]
	v_pk_mul_f32 v[12:13], v[12:13], v[136:137]
	v_pk_mul_f32 v[8:9], v[8:9], v[140:141]
	v_pk_mul_f32 v[4:5], v[4:5], v[144:145]
	v_pk_mul_f32 v[0:1], v[0:1], v[148:149]
	v_pk_mul_f32 v[30:31], v[30:31], v[138:139]
	v_pk_mul_f32 v[26:27], v[26:27], v[142:143]
	v_pk_mul_f32 v[22:23], v[22:23], v[146:147]
	v_pk_mul_f32 v[18:19], v[18:19], v[150:151]
	v_pk_mul_f32 v[28:29], v[28:29], v[136:137]
	v_pk_mul_f32 v[24:25], v[24:25], v[140:141]
	v_pk_mul_f32 v[20:21], v[20:21], v[144:145]
	v_pk_mul_f32 v[16:17], v[16:17], v[148:149]
.LBB6_14:
	v_add_u32_e32 v138, s45, v207
	ds_read_b64_tr_b16 v[156:157], v138 offset:24576
	ds_read_b64_tr_b16 v[158:159], v138 offset:25088
	v_add_f32_e32 v120, v48, v49
	s_waitcnt lgkmcnt(4)
	v_mfma_scale_f32_32x32x64_f8f6f4 v[80:95], v[112:119], v[96:103], v[80:95], v219, v220 op_sel_hi:[0,0,0]
	v_add_f32_e32 v112, v50, v120
	v_add_f32_e32 v112, v51, v112
	v_add_f32_e32 v112, v52, v112
	v_add_f32_e32 v116, v53, v112
	v_cvt_pk_f16_f32 v132, v48, v49
	v_cvt_pk_f16_f32 v133, v50, v51
	ds_read_b64_tr_b16 v[112:113], v138 offset:28672
	ds_read_b64_tr_b16 v[114:115], v138 offset:29184
	v_add_f32_e32 v48, v54, v116
	v_add_f32_e32 v48, v55, v48
	v_add_f32_e32 v48, v56, v48
	v_add_f32_e32 v48, v57, v48
	v_cvt_pk_f16_f32 v134, v52, v53
	v_cvt_pk_f16_f32 v135, v54, v55
	s_waitcnt lgkmcnt(4)
	v_mfma_scale_f32_32x32x64_f8f6f4 v[64:79], v[104:111], v[96:103], v[64:79], v219, v220 op_sel_hi:[0,0,0]
	ds_read_b64_tr_b16 v[104:105], v138 offset:25600
	ds_read_b64_tr_b16 v[106:107], v138 offset:26112
	v_add_f32_e32 v48, v58, v48
	v_add_f32_e32 v48, v59, v48
	v_add_f32_e32 v48, v60, v48
	v_add_f32_e32 v48, v61, v48
	v_cvt_pk_f16_f32 v128, v56, v57
	v_cvt_pk_f16_f32 v129, v58, v59
	ds_read_b64_tr_b16 v[152:153], v138 offset:29696
	ds_read_b64_tr_b16 v[154:155], v138 offset:30208
	v_add_f32_e32 v48, v62, v48
	v_add_f32_e32 v48, v63, v48
	v_add_f32_e32 v48, v32, v48
	v_add_f32_e32 v48, v33, v48
	v_cvt_pk_f16_f32 v130, v60, v61
	v_cvt_pk_f16_f32 v131, v62, v63
	ds_read_b64_tr_b16 v[148:149], v138 offset:26624
	ds_read_b64_tr_b16 v[150:151], v138 offset:27136
	v_add_f32_e32 v48, v34, v48
	v_add_f32_e32 v48, v35, v48
	v_add_f32_e32 v48, v36, v48
	v_add_f32_e32 v48, v37, v48
	v_cvt_pk_f16_f32 v124, v32, v33
	v_cvt_pk_f16_f32 v125, v34, v35
	ds_read_b64_tr_b16 v[144:145], v138 offset:30720
	ds_read_b64_tr_b16 v[146:147], v138 offset:31232
	v_add_f32_e32 v32, v38, v48
	v_add_f32_e32 v32, v39, v32
	v_add_f32_e32 v32, v40, v32
	v_add_f32_e32 v32, v41, v32
	v_cvt_pk_f16_f32 v126, v36, v37
	v_cvt_pk_f16_f32 v127, v38, v39
	ds_read_b64_tr_b16 v[140:141], v138 offset:27648
	ds_read_b64_tr_b16 v[142:143], v138 offset:28160
	v_add_f32_e32 v32, v42, v32
	v_add_f32_e32 v32, v43, v32
	v_add_f32_e32 v32, v44, v32
	v_add_f32_e32 v32, v45, v32
	v_cvt_pk_f16_f32 v120, v40, v41
	v_cvt_pk_f16_f32 v121, v42, v43
	ds_read_b64_tr_b16 v[136:137], v138 offset:31744
	ds_read_b64_tr_b16 v[138:139], v138 offset:32256
	v_add_f32_e32 v32, v46, v32
	v_add_f32_e32 v32, v47, v32
	v_add_f32_e32 v108, 0, v32
	v_cvt_pk_f16_f32 v122, v44, v45
	v_cvt_pk_f16_f32 v123, v46, v47
	s_nop 1
	s_nop 0
	v_add_f32_e32 v185, v185, v108
	v_max_f32_e32 v108, v81, v81
	v_max_f32_e32 v109, v80, v80
	v_max_f32_e32 v108, v109, v108
	v_max3_f32 v109, v82, v83, v65
	v_max3_f32 v108, v108, v64, v66
	v_max3_f32 v108, v108, v67, v84
	v_max3_f32 v109, v109, v86, v87
	v_max3_f32 v108, v108, v85, v68
	v_max3_f32 v109, v109, v70, v71
	v_max3_f32 v108, v108, v69, v88
	v_max3_f32 v109, v109, v90, v91
	s_waitcnt vmcnt(0)
	s_barrier
	v_max3_f32 v108, v108, v89, v72
	v_max3_f32 v109, v109, v74, v75
	ds_read_b128 v[48:51], v221 offset:32768
	ds_read_b128 v[32:35], v161 offset:32768
	ds_read_b128 v[52:55], v184 offset:32768
	ds_read_b128 v[36:39], v211 offset:32768
	ds_read_b128 v[56:59], v212 offset:32768
	ds_read_b128 v[40:43], v213 offset:32768
	ds_read_b128 v[60:63], v214 offset:32768
	ds_read_b128 v[44:47], v215 offset:32768
	v_max3_f32 v108, v108, v73, v92
	v_max3_f32 v109, v109, v94, v95
	v_max3_f32 v108, v108, v93, v76
	v_max3_f32 v109, v109, v78, v79
	v_max3_f32 v108, v108, v77, v109
	v_mov_b32_e32 v109, v108
	s_nop 1
	v_permlane32_swap_b32_e32 v108, v109
	v_max_f32_e32 v109, v109, v109
	v_max_f32_e32 v108, v108, v108
	v_max_f32_e32 v108, v108, v109
	v_fma_f32 v108, v108, s41, -v208
	v_cmp_lt_f32_e32 vcc, s29, v108
	s_cmp_lg_u64 vcc, 0
	s_cselect_b64 s[24:25], -1, 0
	s_cbranch_vccnz .LBB6_24
.LBB6_15:
	s_waitcnt lgkmcnt(14)
	v_mfma_f32_32x32x16_f16 v[0:15], v[132:135], v[156:159], v[0:15]
	v_fma_f32 v80, v80, s41, -v208
	v_fma_f32 v81, v81, s41, -v208
	v_fma_f32 v82, v82, s41, -v208
	v_fma_f32 v83, v83, s41, -v208
	v_exp_f32_e32 v80, v80
	v_exp_f32_e32 v81, v81
	v_exp_f32_e32 v82, v82
	v_exp_f32_e32 v83, v83
	s_and_b64 vcc, exec, s[4:5]
	s_nop 0
	v_lshl_add_u64 v[108:109], v[180:181], 0, s[20:21]
	s_add_i32 s26, s28, s39
	s_mov_b32 m0, s26
	s_nop 0
	global_load_lds_dwordx4 v[108:109], off
.LBB6_17:
	s_add_i32 s26, s28, 0x2000
	s_cmpk_lg_i32 s28, 0x4000
	s_cselect_b32 s45, s26, 0
	v_mfma_f32_32x32x16_f16 v[16:31], v[132:135], v[112:115], v[16:31]
	v_fma_f32 v84, v84, s41, -v208
	v_fma_f32 v85, v85, s41, -v208
	v_fma_f32 v86, v86, s41, -v208
	v_fma_f32 v87, v87, s41, -v208
	v_exp_f32_e32 v84, v84
	v_exp_f32_e32 v85, v85
	v_exp_f32_e32 v86, v86
	v_exp_f32_e32 v87, v87
	v_lshl_add_u64 v[182:183], v[182:183], 0, s[12:13]
	s_add_i32 s26, s45, s37
	s_mov_b32 m0, s26
	s_nop 0
	global_load_lds_dwordx4 v[182:183], off
	v_lshl_add_u64 v[226:227], v[182:183], 0, s[58:59]
	s_add_i32 m0, s26, 0x6800
	s_nop 0
	global_load_lds_dwordx4 v[226:227], off
	s_waitcnt lgkmcnt(0)
	v_lshl_add_u64 v[108:109], v[186:187], 0, s[22:23]
	v_lshl_add_u64 v[108:109], v[108:109], 0, s[62:63]
	s_add_i32 m0, s38, s64
	s_nop 0
	global_load_lds_dwordx4 v[108:109], off nt
	v_add_u32_e32 v108, s45, v216
	v_add_u32_e32 v109, v108, v217
	v_add_u32_e32 v108, v108, v218
	ds_read_b128 v[112:115], v109
	ds_read_b128 v[116:119], v108
	v_mfma_f32_32x32x16_f16 v[0:15], v[128:131], v[104:107], v[0:15]
	v_fma_f32 v88, v88, s41, -v208
	v_fma_f32 v89, v89, s41, -v208
	v_fma_f32 v90, v90, s41, -v208
	v_fma_f32 v91, v91, s41, -v208
	v_exp_f32_e32 v88, v88
	v_exp_f32_e32 v89, v89
	v_exp_f32_e32 v90, v90
	v_exp_f32_e32 v91, v91
	v_lshl_add_u64 v[104:105], v[188:189], 0, s[22:23]
	v_lshl_add_u64 v[104:105], v[104:105], 0, s[62:63]
	s_add_i32 m0, s30, s64
	s_nop 0
	global_load_lds_dwordx4 v[104:105], off nt
	ds_read_b128 v[104:107], v109 offset:2048
	ds_read_b128 v[108:111], v108 offset:2048
	v_mfma_f32_32x32x16_f16 v[16:31], v[128:131], v[152:155], v[16:31]
	v_fma_f32 v92, v92, s41, -v208
	v_fma_f32 v93, v93, s41, -v208
	v_fma_f32 v94, v94, s41, -v208
	v_fma_f32 v95, v95, s41, -v208
	v_exp_f32_e32 v92, v92
	v_exp_f32_e32 v93, v93
	v_exp_f32_e32 v94, v94
	v_exp_f32_e32 v95, v95
	v_lshl_add_u64 v[128:129], v[190:191], 0, s[22:23]
	v_lshl_add_u64 v[128:129], v[128:129], 0, s[62:63]
	s_add_i32 m0, s31, s64
	s_nop 0
	global_load_lds_dwordx4 v[128:129], off nt
	v_mfma_f32_32x32x16_f16 v[0:15], v[124:127], v[148:151], v[0:15]
	v_fma_f32 v64, v64, s41, -v208
	v_fma_f32 v65, v65, s41, -v208
	v_fma_f32 v66, v66, s41, -v208
	v_fma_f32 v67, v67, s41, -v208
	v_exp_f32_e32 v64, v64
	v_exp_f32_e32 v65, v65
	v_exp_f32_e32 v66, v66
	v_exp_f32_e32 v67, v67
	v_lshl_add_u64 v[128:129], v[192:193], 0, s[22:23]
	v_lshl_add_u64 v[128:129], v[128:129], 0, s[62:63]
	s_add_i32 m0, s34, s64
	s_nop 0
	global_load_lds_dwordx4 v[128:129], off nt
	s_waitcnt lgkmcnt(14)
	v_mfma_f32_32x32x16_f16 v[16:31], v[124:127], v[144:147], v[16:31]
	v_fma_f32 v68, v68, s41, -v208
	v_fma_f32 v69, v69, s41, -v208
	v_fma_f32 v70, v70, s41, -v208
	v_fma_f32 v71, v71, s41, -v208
	v_exp_f32_e32 v68, v68
	v_exp_f32_e32 v69, v69
	v_exp_f32_e32 v70, v70
	v_exp_f32_e32 v71, v71
	v_mfma_f32_32x32x16_f16 v[0:15], v[120:123], v[140:143], v[0:15]
	v_fma_f32 v72, v72, s41, -v208
	v_fma_f32 v73, v73, s41, -v208
	v_fma_f32 v74, v74, s41, -v208
	v_fma_f32 v75, v75, s41, -v208
	v_exp_f32_e32 v72, v72
	v_exp_f32_e32 v73, v73
	v_exp_f32_e32 v74, v74
	v_exp_f32_e32 v75, v75
	s_waitcnt lgkmcnt(12)
	v_mfma_f32_32x32x16_f16 v[16:31], v[120:123], v[136:139], v[16:31]
	v_fma_f32 v76, v76, s41, -v208
	v_fma_f32 v77, v77, s41, -v208
	v_fma_f32 v78, v78, s41, -v208
	v_fma_f32 v79, v79, s41, -v208
	v_exp_f32_e32 v76, v76
	v_exp_f32_e32 v77, v77
	v_exp_f32_e32 v78, v78
	v_exp_f32_e32 v79, v79
	s_waitcnt vmcnt(7) lgkmcnt(0)
	s_barrier
	s_andn2_b64 vcc, exec, s[24:25]
	s_cbranch_vccnz .LBB6_19
	ds_read_b128 v[136:139], v205 offset:49248
	ds_read_b128 v[140:143], v205 offset:49216
	ds_read_b128 v[144:147], v205 offset:49184
	ds_read_b128 v[148:151], v205 offset:49152
	s_waitcnt lgkmcnt(3)
	v_pk_mul_f32 v[14:15], v[14:15], v[138:139]
	s_waitcnt lgkmcnt(2)
	v_pk_mul_f32 v[10:11], v[10:11], v[142:143]
	s_waitcnt lgkmcnt(1)
	v_pk_mul_f32 v[6:7], v[6:7], v[146:147]
	s_waitcnt lgkmcnt(0)
	v_pk_mul_f32 v[2:3], v[2:3], v[150:151]
	v_pk_mul_f32 v[12:13], v[12:13], v[136:137]
	v_pk_mul_f32 v[8:9], v[8:9], v[140:141]
	v_pk_mul_f32 v[4:5], v[4:5], v[144:145]
	v_pk_mul_f32 v[0:1], v[0:1], v[148:149]
	v_pk_mul_f32 v[30:31], v[30:31], v[138:139]
	v_pk_mul_f32 v[26:27], v[26:27], v[142:143]
	v_pk_mul_f32 v[22:23], v[22:23], v[146:147]
	v_pk_mul_f32 v[18:19], v[18:19], v[150:151]
	v_pk_mul_f32 v[28:29], v[28:29], v[136:137]
	v_pk_mul_f32 v[24:25], v[24:25], v[140:141]
	v_pk_mul_f32 v[20:21], v[20:21], v[144:145]
	v_pk_mul_f32 v[16:17], v[16:17], v[148:149]

.LBB6_27:
	ds_read_b64_tr_b16 v[156:157], v207 offset:32768
	ds_read_b64_tr_b16 v[158:159], v207 offset:33280
	v_add_f32_e32 v120, v80, v81
	v_mov_b32_e32 v121, 0x7f7f7f7f
	v_mov_b32_e32 v124, 0x7c7c7c7c
	s_waitcnt lgkmcnt(4)
	v_mfma_scale_f32_32x32x64_f8f6f4 v[48:63], v[112:119], v[96:103], v[48:63], v121, v124 op_sel_hi:[0,0,0]
	v_add_f32_e32 v112, v82, v120
	v_add_f32_e32 v112, v83, v112
	v_add_f32_e32 v112, v84, v112
	v_add_f32_e32 v116, v85, v112
	v_cvt_pk_f16_f32 v132, v80, v81
	v_cvt_pk_f16_f32 v133, v82, v83
	ds_read_b64_tr_b16 v[112:113], v207 offset:36864
	ds_read_b64_tr_b16 v[114:115], v207 offset:37376
	v_add_f32_e32 v80, v86, v116
	v_add_f32_e32 v80, v87, v80
	v_add_f32_e32 v80, v88, v80
	v_add_f32_e32 v80, v89, v80
	v_cvt_pk_f16_f32 v134, v84, v85
	v_cvt_pk_f16_f32 v135, v86, v87
	s_waitcnt lgkmcnt(4)
	v_mfma_scale_f32_32x32x64_f8f6f4 v[32:47], v[104:111], v[96:103], v[32:47], v121, v124 op_sel_hi:[0,0,0]
	ds_read_b64_tr_b16 v[104:105], v207 offset:33792
	ds_read_b64_tr_b16 v[106:107], v207 offset:34304
	v_add_f32_e32 v80, v90, v80
	v_add_f32_e32 v80, v91, v80
	v_add_f32_e32 v80, v92, v80
	v_add_f32_e32 v80, v93, v80
	v_cvt_pk_f16_f32 v128, v88, v89
	v_cvt_pk_f16_f32 v129, v90, v91
	ds_read_b64_tr_b16 v[152:153], v207 offset:37888
	ds_read_b64_tr_b16 v[154:155], v207 offset:38400
	v_add_f32_e32 v80, v94, v80
	v_add_f32_e32 v80, v95, v80
	v_add_f32_e32 v80, v64, v80
	v_add_f32_e32 v80, v65, v80
	v_cvt_pk_f16_f32 v130, v92, v93
	v_cvt_pk_f16_f32 v131, v94, v95
	ds_read_b64_tr_b16 v[148:149], v207 offset:34816
	ds_read_b64_tr_b16 v[150:151], v207 offset:35328
	v_add_f32_e32 v80, v66, v80
	v_add_f32_e32 v80, v67, v80
	v_add_f32_e32 v80, v68, v80
	v_add_f32_e32 v80, v69, v80
	v_cvt_pk_f16_f32 v124, v64, v65
	v_cvt_pk_f16_f32 v125, v66, v67
	ds_read_b64_tr_b16 v[144:145], v207 offset:38912
	ds_read_b64_tr_b16 v[146:147], v207 offset:39424
	v_add_f32_e32 v64, v70, v80
	v_add_f32_e32 v64, v71, v64
	v_add_f32_e32 v64, v72, v64
	v_add_f32_e32 v64, v73, v64
	v_cvt_pk_f16_f32 v126, v68, v69
	v_cvt_pk_f16_f32 v127, v70, v71
	ds_read_b64_tr_b16 v[140:141], v207 offset:35840
	ds_read_b64_tr_b16 v[142:143], v207 offset:36352
	v_add_f32_e32 v64, v74, v64
	v_add_f32_e32 v64, v75, v64
	v_add_f32_e32 v64, v76, v64
	v_add_f32_e32 v64, v77, v64
	v_cvt_pk_f16_f32 v120, v72, v73
	v_cvt_pk_f16_f32 v121, v74, v75
	ds_read_b64_tr_b16 v[136:137], v207 offset:39936
	ds_read_b64_tr_b16 v[138:139], v207 offset:40448
	v_add_f32_e32 v64, v78, v64
	v_add_f32_e32 v64, v79, v64
	v_add_f32_e32 v108, 0, v64
	v_cvt_pk_f16_f32 v122, v76, v77
	v_cvt_pk_f16_f32 v123, v78, v79
	s_nop 1
	s_nop 0
	v_add_f32_e32 v180, v185, v108
	v_max_f32_e32 v108, v49, v49
	v_max_f32_e32 v109, v48, v48
	v_max_f32_e32 v108, v109, v108
	v_max3_f32 v109, v50, v51, v33
	v_max3_f32 v108, v108, v32, v34
	v_max3_f32 v108, v108, v35, v52
	v_max3_f32 v109, v109, v54, v55
	v_max3_f32 v108, v108, v53, v36
	v_max3_f32 v109, v109, v38, v39
	v_max3_f32 v108, v108, v37, v56
	v_max3_f32 v109, v109, v58, v59
	s_waitcnt vmcnt(0)
	s_barrier
	v_max3_f32 v108, v108, v57, v40
	v_max3_f32 v109, v109, v42, v43
	ds_read_b128 v[80:83], v221
	ds_read_b128 v[64:67], v161
	ds_read_b128 v[84:87], v184
	ds_read_b128 v[68:71], v211
	ds_read_b128 v[88:91], v212
	ds_read_b128 v[72:75], v213
	ds_read_b128 v[92:95], v214
	ds_read_b128 v[76:79], v215
	v_max3_f32 v108, v108, v41, v60
	v_max3_f32 v109, v109, v62, v63
	v_max3_f32 v108, v108, v61, v44
	v_max3_f32 v109, v109, v46, v47
	v_max3_f32 v108, v108, v45, v109
	v_mov_b32_e32 v109, v108
	s_nop 1
	v_permlane32_swap_b32_e32 v108, v109
	v_max_f32_e32 v109, v109, v109
	v_max_f32_e32 v108, v108, v108
	v_max_f32_e32 v108, v108, v109
	s_mov_b32 s8, 0x3fb8aa3b
	v_fma_f32 v108, v108, s8, -v208
	s_mov_b32 s2, 0x41000000
	v_cmp_lt_f32_e32 vcc, s2, v108
	s_cmp_lg_u64 vcc, 0
	s_cselect_b64 s[2:3], -1, 0
	s_cbranch_vccnz .LBB6_39
.LBB6_28:
	s_waitcnt lgkmcnt(14)
	v_mfma_f32_32x32x16_f16 v[0:15], v[132:135], v[156:159], v[0:15]
	v_fma_f32 v48, v48, s8, -v208
	v_fma_f32 v49, v49, s8, -v208
	v_fma_f32 v50, v50, s8, -v208
	v_fma_f32 v51, v51, s8, -v208
	v_exp_f32_e32 v48, v48
	v_exp_f32_e32 v49, v49
	v_exp_f32_e32 v50, v50
	v_exp_f32_e32 v51, v51
	v_mfma_f32_32x32x16_f16 v[16:31], v[132:135], v[112:115], v[16:31]
	v_fma_f32 v52, v52, s8, -v208
	v_fma_f32 v53, v53, s8, -v208
	v_fma_f32 v54, v54, s8, -v208
	v_fma_f32 v55, v55, s8, -v208
	v_exp_f32_e32 v52, v52
	v_exp_f32_e32 v53, v53
	v_exp_f32_e32 v54, v54
	v_exp_f32_e32 v55, v55
	s_mov_b64 s[4:5], 0x780000
	v_lshl_add_u64 v[108:109], v[162:163], 0, s[4:5]
	s_mov_b32 m0, s37
	s_nop 0
	global_load_lds_dwordx4 v[108:109], off
	v_lshl_add_u64 v[226:227], v[108:109], 0, s[58:59]
	s_add_i32 m0, s37, 0x6800
	s_nop 0
	global_load_lds_dwordx4 v[226:227], off
	s_mov_b64 s[4:5], 0x1f00
	s_waitcnt lgkmcnt(0)
	v_lshl_add_u64 v[108:109], v[164:165], 0, s[4:5]
	v_lshl_add_u64 v[108:109], v[108:109], 0, s[62:63]
	s_add_i32 m0, s38, s65
	s_nop 0
	global_load_lds_dwordx4 v[108:109], off nt
	ds_read_b128 v[112:115], v209
	ds_read_b128 v[116:119], v210
	v_mfma_f32_32x32x16_f16 v[0:15], v[128:131], v[104:107], v[0:15]
	v_fma_f32 v56, v56, s8, -v208
	v_fma_f32 v57, v57, s8, -v208
	v_fma_f32 v58, v58, s8, -v208
	v_fma_f32 v59, v59, s8, -v208
	v_exp_f32_e32 v56, v56
	v_exp_f32_e32 v57, v57
	v_exp_f32_e32 v58, v58
	v_exp_f32_e32 v59, v59
	s_cmp_lg_u32 0, -1
	s_cselect_b32 s9, 0, 0
	s_add_i32 s7, s9, s7
	v_lshl_add_u64 v[104:105], v[178:179], 0, s[4:5]
	v_lshl_add_u64 v[104:105], v[104:105], 0, s[62:63]
	s_add_i32 s9, s7, 0x14c00
	s_add_i32 m0, s9, s65
	s_nop 0
	global_load_lds_dwordx4 v[104:105], off nt
	ds_read_b128 v[104:107], v209 offset:2048
	ds_read_b128 v[108:111], v210 offset:2048
	v_mfma_f32_32x32x16_f16 v[16:31], v[128:131], v[152:155], v[16:31]
	v_fma_f32 v60, v60, s8, -v208
	v_fma_f32 v61, v61, s8, -v208
	v_fma_f32 v62, v62, s8, -v208
	v_fma_f32 v63, v63, s8, -v208
	v_exp_f32_e32 v60, v60
	v_exp_f32_e32 v61, v61
	v_exp_f32_e32 v62, v62
	v_exp_f32_e32 v63, v63
	v_lshl_add_u64 v[128:129], v[176:177], 0, s[4:5]
	v_lshl_add_u64 v[128:129], v[128:129], 0, s[62:63]
	s_add_i32 s9, s7, 0x15000
	s_add_i32 m0, s9, s65
	s_nop 0
	global_load_lds_dwordx4 v[128:129], off nt
	v_mfma_f32_32x32x16_f16 v[0:15], v[124:127], v[148:151], v[0:15]
	v_fma_f32 v32, v32, s8, -v208
	v_fma_f32 v33, v33, s8, -v208
	v_fma_f32 v34, v34, s8, -v208
	v_fma_f32 v35, v35, s8, -v208
	v_exp_f32_e32 v32, v32
	v_exp_f32_e32 v33, v33
	v_exp_f32_e32 v34, v34
	v_exp_f32_e32 v35, v35
	v_lshl_add_u64 v[128:129], v[174:175], 0, s[4:5]
	v_lshl_add_u64 v[128:129], v[128:129], 0, s[62:63]
	s_add_i32 s9, s7, 0x15400
	s_add_i32 m0, s9, s65
	s_nop 0
	global_load_lds_dwordx4 v[128:129], off nt
	s_waitcnt lgkmcnt(14)
	v_mfma_f32_32x32x16_f16 v[16:31], v[124:127], v[144:147], v[16:31]
	v_fma_f32 v36, v36, s8, -v208
	v_fma_f32 v37, v37, s8, -v208
	v_fma_f32 v38, v38, s8, -v208
	v_fma_f32 v39, v39, s8, -v208
	v_exp_f32_e32 v36, v36
	v_exp_f32_e32 v37, v37
	v_exp_f32_e32 v38, v38
	v_exp_f32_e32 v39, v39
	s_add_i32 s9, s7, 0x15800
	v_mfma_f32_32x32x16_f16 v[0:15], v[120:123], v[140:143], v[0:15]
	v_fma_f32 v40, v40, s8, -v208
	v_fma_f32 v41, v41, s8, -v208
	v_fma_f32 v42, v42, s8, -v208
	v_fma_f32 v43, v43, s8, -v208
	v_exp_f32_e32 v40, v40
	v_exp_f32_e32 v41, v41
	v_exp_f32_e32 v42, v42
	v_exp_f32_e32 v43, v43
	s_add_i32 s9, s7, 0x15c00
	s_waitcnt lgkmcnt(12)
	v_mfma_f32_32x32x16_f16 v[16:31], v[120:123], v[136:139], v[16:31]
	v_fma_f32 v44, v44, s8, -v208
	v_fma_f32 v45, v45, s8, -v208
	v_fma_f32 v46, v46, s8, -v208
	v_fma_f32 v47, v47, s8, -v208
	v_exp_f32_e32 v44, v44
	v_exp_f32_e32 v45, v45
	v_exp_f32_e32 v46, v46
	v_exp_f32_e32 v47, v47
	s_add_i32 s8, s7, 0x16000
	s_add_i32 s7, s7, 0x16400
	s_waitcnt vmcnt(6) lgkmcnt(0)
	s_barrier
	s_andn2_b64 vcc, exec, s[2:3]
	s_cbranch_vccnz .LBB6_30
	ds_read_b128 v[136:139], v205 offset:49248
	ds_read_b128 v[140:143], v205 offset:49216
	ds_read_b128 v[144:147], v205 offset:49184
	ds_read_b128 v[148:151], v205 offset:49152
	s_waitcnt lgkmcnt(3)
	v_pk_mul_f32 v[14:15], v[14:15], v[138:139]
	s_waitcnt lgkmcnt(2)
	v_pk_mul_f32 v[10:11], v[10:11], v[142:143]
	s_waitcnt lgkmcnt(1)
	v_pk_mul_f32 v[6:7], v[6:7], v[146:147]
	s_waitcnt lgkmcnt(0)
	v_pk_mul_f32 v[2:3], v[2:3], v[150:151]
	v_pk_mul_f32 v[12:13], v[12:13], v[136:137]
	v_pk_mul_f32 v[8:9], v[8:9], v[140:141]
	v_pk_mul_f32 v[4:5], v[4:5], v[144:145]
	v_pk_mul_f32 v[0:1], v[0:1], v[148:149]
	v_pk_mul_f32 v[30:31], v[30:31], v[138:139]
	v_pk_mul_f32 v[26:27], v[26:27], v[142:143]
	v_pk_mul_f32 v[22:23], v[22:23], v[146:147]
	v_pk_mul_f32 v[18:19], v[18:19], v[150:151]
	v_pk_mul_f32 v[28:29], v[28:29], v[136:137]
	v_pk_mul_f32 v[24:25], v[24:25], v[140:141]
	v_pk_mul_f32 v[20:21], v[20:21], v[144:145]
	v_pk_mul_f32 v[16:17], v[16:17], v[148:149]
.LBB6_30:
	ds_read_b64_tr_b16 v[152:153], v207 offset:40960
	ds_read_b64_tr_b16 v[154:155], v207 offset:41472
	v_add_f32_e32 v120, v48, v49
	v_mov_b32_e32 v121, 0x7f7f7f7f
	v_mov_b32_e32 v124, 0x7c7c7c7c
	s_waitcnt lgkmcnt(4)
	v_mfma_scale_f32_32x32x64_f8f6f4 v[80:95], v[112:119], v[96:103], v[80:95], v121, v124 op_sel_hi:[0,0,0]
	v_add_f32_e32 v112, v50, v120
	v_add_f32_e32 v112, v51, v112
	v_add_f32_e32 v112, v52, v112
	v_add_f32_e32 v116, v53, v112
	v_cvt_pk_f16_f32 v132, v48, v49
	v_cvt_pk_f16_f32 v133, v50, v51
	ds_read_b64_tr_b16 v[112:113], v207 offset:45056
	ds_read_b64_tr_b16 v[114:115], v207 offset:45568
	v_add_f32_e32 v48, v54, v116
	v_add_f32_e32 v48, v55, v48
	v_add_f32_e32 v48, v56, v48
	v_add_f32_e32 v48, v57, v48
	v_cvt_pk_f16_f32 v134, v52, v53
	v_cvt_pk_f16_f32 v135, v54, v55
	s_waitcnt lgkmcnt(4)
	v_mfma_scale_f32_32x32x64_f8f6f4 v[64:79], v[104:111], v[96:103], v[64:79], v121, v124 op_sel_hi:[0,0,0]
	ds_read_b64_tr_b16 v[104:105], v207 offset:41984
	ds_read_b64_tr_b16 v[106:107], v207 offset:42496
	v_add_f32_e32 v48, v58, v48
	v_add_f32_e32 v48, v59, v48
	v_add_f32_e32 v48, v60, v48
	v_add_f32_e32 v48, v61, v48
	v_cvt_pk_f16_f32 v128, v56, v57
	v_cvt_pk_f16_f32 v129, v58, v59
	ds_read_b64_tr_b16 v[156:157], v207 offset:46080
	ds_read_b64_tr_b16 v[158:159], v207 offset:46592
	v_add_f32_e32 v48, v62, v48
	v_add_f32_e32 v48, v63, v48
	v_add_f32_e32 v48, v32, v48
	v_add_f32_e32 v48, v33, v48
	v_cvt_pk_f16_f32 v130, v60, v61
	v_cvt_pk_f16_f32 v131, v62, v63
	ds_read_b64_tr_b16 v[148:149], v207 offset:43008
	ds_read_b64_tr_b16 v[150:151], v207 offset:43520
	v_add_f32_e32 v48, v34, v48
	v_add_f32_e32 v48, v35, v48
	v_add_f32_e32 v48, v36, v48
	v_add_f32_e32 v48, v37, v48
	v_cvt_pk_f16_f32 v124, v32, v33
	v_cvt_pk_f16_f32 v125, v34, v35
	ds_read_b64_tr_b16 v[144:145], v207 offset:47104
	ds_read_b64_tr_b16 v[146:147], v207 offset:47616
	v_add_f32_e32 v32, v38, v48
	v_add_f32_e32 v32, v39, v32
	v_add_f32_e32 v32, v40, v32
	v_add_f32_e32 v32, v41, v32
	v_cvt_pk_f16_f32 v126, v36, v37
	v_cvt_pk_f16_f32 v127, v38, v39
	ds_read_b64_tr_b16 v[140:141], v207 offset:44032
	ds_read_b64_tr_b16 v[142:143], v207 offset:44544
	v_add_f32_e32 v32, v42, v32
	v_add_f32_e32 v32, v43, v32
	v_add_f32_e32 v32, v44, v32
	v_add_f32_e32 v32, v45, v32
	v_cvt_pk_f16_f32 v120, v40, v41
	v_cvt_pk_f16_f32 v121, v42, v43
	ds_read_b64_tr_b16 v[136:137], v207 offset:48128
	ds_read_b64_tr_b16 v[138:139], v207 offset:48640
	v_add_f32_e32 v32, v46, v32
	v_add_f32_e32 v32, v47, v32
	v_add_f32_e32 v32, 0, v32
	v_cvt_pk_f16_f32 v122, v44, v45
	v_cvt_pk_f16_f32 v123, v46, v47
	s_nop 1
	s_waitcnt vmcnt(0)
	s_barrier
	s_nop 0
	v_add_f32_e32 v164, v180, v32
	v_max_f32_e32 v108, v81, v81
	v_max_f32_e32 v109, v80, v80
	v_max_f32_e32 v108, v109, v108
	v_max3_f32 v109, v82, v83, v65
	v_max3_f32 v108, v108, v64, v66
	v_max3_f32 v108, v108, v67, v84
	v_max3_f32 v109, v109, v86, v87
	v_max3_f32 v108, v108, v85, v68
	v_max3_f32 v109, v109, v70, v71
	v_max3_f32 v108, v108, v69, v88
	v_max3_f32 v109, v109, v90, v91
	v_max3_f32 v108, v108, v89, v72
	v_max3_f32 v109, v109, v74, v75
	ds_read_b128 v[48:51], v221 offset:32768
	ds_read_b128 v[32:35], v161 offset:32768
	ds_read_b128 v[52:55], v184 offset:32768
	ds_read_b128 v[36:39], v211 offset:32768
	ds_read_b128 v[56:59], v212 offset:32768
	ds_read_b128 v[40:43], v213 offset:32768
	ds_read_b128 v[60:63], v214 offset:32768
	ds_read_b128 v[44:47], v215 offset:32768
	v_max3_f32 v108, v108, v73, v92
	v_max3_f32 v109, v109, v94, v95
	v_max3_f32 v108, v108, v93, v76
	v_max3_f32 v109, v109, v78, v79
	v_max3_f32 v108, v108, v77, v109
	v_mov_b32_e32 v109, v108
	s_nop 1
	v_permlane32_swap_b32_e32 v108, v109
	v_max_f32_e32 v109, v109, v109
	v_max_f32_e32 v108, v108, v108
	v_max_f32_e32 v108, v108, v109
	s_mov_b32 s7, 0x3fb8aa3b
	v_fma_f32 v108, v108, s7, -v208
	s_mov_b32 s2, 0x41000000
	v_cmp_lt_f32_e32 vcc, s2, v108
	s_cmp_lg_u64 vcc, 0
	s_cselect_b64 s[2:3], -1, 0
	s_cbranch_vccnz .LBB6_42
.LBB6_31:
	s_waitcnt lgkmcnt(14)
	v_mfma_f32_32x32x16_f16 v[0:15], v[132:135], v[152:155], v[0:15]
	v_fma_f32 v80, v80, s7, -v208
	v_fma_f32 v81, v81, s7, -v208
	v_fma_f32 v82, v82, s7, -v208
	v_fma_f32 v83, v83, s7, -v208
	v_exp_f32_e32 v80, v80
	v_exp_f32_e32 v81, v81
	v_exp_f32_e32 v82, v82
	v_exp_f32_e32 v83, v83
	v_mfma_f32_32x32x16_f16 v[16:31], v[132:135], v[112:115], v[16:31]
	v_fma_f32 v84, v84, s7, -v208
	v_fma_f32 v85, v85, s7, -v208
	v_fma_f32 v86, v86, s7, -v208
	v_fma_f32 v87, v87, s7, -v208
	v_exp_f32_e32 v84, v84
	v_exp_f32_e32 v85, v85
	v_exp_f32_e32 v86, v86
	v_exp_f32_e32 v87, v87
	s_mov_b64 s[4:5], 0x7c0000
	s_cmp_lg_u32 0, -1
	v_lshl_add_u64 v[108:109], v[162:163], 0, s[4:5]
	s_cselect_b32 s4, 0, 0
	s_add_i32 s4, s4, s36
	s_add_i32 s4, s4, 0x8000
	s_mov_b32 m0, s4
	s_nop 0
	global_load_lds_dwordx4 v[108:109], off
	v_lshl_add_u64 v[226:227], v[108:109], 0, s[58:59]
	s_add_i32 m0, s4, 0x6800
	s_nop 0
	global_load_lds_dwordx4 v[226:227], off
	ds_read_b128 v[112:115], v209 offset:8192
	ds_read_b128 v[116:119], v210 offset:8192
	v_mfma_f32_32x32x16_f16 v[0:15], v[128:131], v[104:107], v[0:15]
	v_fma_f32 v88, v88, s7, -v208
	v_fma_f32 v89, v89, s7, -v208
	v_fma_f32 v90, v90, s7, -v208
	v_fma_f32 v91, v91, s7, -v208
	v_exp_f32_e32 v88, v88
	v_exp_f32_e32 v89, v89
	v_exp_f32_e32 v90, v90
	v_exp_f32_e32 v91, v91
	ds_read_b128 v[104:107], v209 offset:10240
	ds_read_b128 v[108:111], v210 offset:10240
	v_mfma_f32_32x32x16_f16 v[16:31], v[128:131], v[156:159], v[16:31]
	v_fma_f32 v92, v92, s7, -v208
	v_fma_f32 v93, v93, s7, -v208
	v_fma_f32 v94, v94, s7, -v208
	v_fma_f32 v95, v95, s7, -v208
	v_exp_f32_e32 v92, v92
	v_exp_f32_e32 v93, v93
	v_exp_f32_e32 v94, v94
	v_exp_f32_e32 v95, v95
	v_mfma_f32_32x32x16_f16 v[0:15], v[124:127], v[148:151], v[0:15]
	v_fma_f32 v64, v64, s7, -v208
	v_fma_f32 v65, v65, s7, -v208
	v_fma_f32 v66, v66, s7, -v208
	v_fma_f32 v67, v67, s7, -v208
	v_exp_f32_e32 v64, v64
	v_exp_f32_e32 v65, v65
	v_exp_f32_e32 v66, v66
	v_exp_f32_e32 v67, v67
	s_waitcnt lgkmcnt(14)
	v_mfma_f32_32x32x16_f16 v[16:31], v[124:127], v[144:147], v[16:31]
	v_fma_f32 v68, v68, s7, -v208
	v_fma_f32 v69, v69, s7, -v208
	v_fma_f32 v70, v70, s7, -v208
	v_fma_f32 v71, v71, s7, -v208
	v_exp_f32_e32 v68, v68
	v_exp_f32_e32 v69, v69
	v_exp_f32_e32 v70, v70
	v_exp_f32_e32 v71, v71
	v_mfma_f32_32x32x16_f16 v[0:15], v[120:123], v[140:143], v[0:15]
	v_fma_f32 v72, v72, s7, -v208
	v_fma_f32 v73, v73, s7, -v208
	v_fma_f32 v74, v74, s7, -v208
	v_fma_f32 v75, v75, s7, -v208
	v_exp_f32_e32 v72, v72
	v_exp_f32_e32 v73, v73
	v_exp_f32_e32 v74, v74
	v_exp_f32_e32 v75, v75
	s_waitcnt lgkmcnt(12)
	v_mfma_f32_32x32x16_f16 v[16:31], v[120:123], v[136:139], v[16:31]
	v_fma_f32 v76, v76, s7, -v208
	v_fma_f32 v77, v77, s7, -v208
	v_fma_f32 v78, v78, s7, -v208
	v_fma_f32 v79, v79, s7, -v208
	v_exp_f32_e32 v76, v76
	v_exp_f32_e32 v77, v77
	v_exp_f32_e32 v78, v78
	v_exp_f32_e32 v79, v79
	s_waitcnt vmcnt(0) lgkmcnt(0)
	s_barrier
	s_andn2_b64 vcc, exec, s[2:3]
	s_cbranch_vccnz .LBB6_33
	ds_read_b128 v[136:139], v205 offset:49248
	ds_read_b128 v[140:143], v205 offset:49216
	ds_read_b128 v[144:147], v205 offset:49184
	ds_read_b128 v[148:151], v205 offset:49152
	s_waitcnt lgkmcnt(3)
	v_pk_mul_f32 v[14:15], v[14:15], v[138:139]
	s_waitcnt lgkmcnt(2)
	v_pk_mul_f32 v[10:11], v[10:11], v[142:143]
	s_waitcnt lgkmcnt(1)
	v_pk_mul_f32 v[6:7], v[6:7], v[146:147]
	s_waitcnt lgkmcnt(0)
	v_pk_mul_f32 v[2:3], v[2:3], v[150:151]
	v_pk_mul_f32 v[12:13], v[12:13], v[136:137]
	v_pk_mul_f32 v[8:9], v[8:9], v[140:141]
	v_pk_mul_f32 v[4:5], v[4:5], v[144:145]
	v_pk_mul_f32 v[0:1], v[0:1], v[148:149]
	v_pk_mul_f32 v[30:31], v[30:31], v[138:139]
	v_pk_mul_f32 v[26:27], v[26:27], v[142:143]
	v_pk_mul_f32 v[22:23], v[22:23], v[146:147]
	v_pk_mul_f32 v[18:19], v[18:19], v[150:151]
	v_pk_mul_f32 v[28:29], v[28:29], v[136:137]
	v_pk_mul_f32 v[24:25], v[24:25], v[140:141]
	v_pk_mul_f32 v[20:21], v[20:21], v[144:145]
	v_pk_mul_f32 v[16:17], v[16:17], v[148:149]

.LBB6_36:
	v_add_f32_e32 v64, v48, v49
	v_add_f32_e32 v64, v50, v64
	v_add_f32_e32 v64, v51, v64
	v_add_f32_e32 v64, v52, v64
	v_add_f32_e32 v68, v53, v64
	v_cvt_pk_f16_f32 v48, v48, v49
	v_cvt_pk_f16_f32 v49, v50, v51
	v_cvt_pk_f16_f32 v50, v52, v53
	v_cvt_pk_f16_f32 v51, v54, v55
	ds_read_b64_tr_b16 v[64:65], v207 offset:32768
	ds_read_b64_tr_b16 v[66:67], v207 offset:33280
	v_add_f32_e32 v52, v54, v68
	v_add_f32_e32 v68, v55, v52
	ds_read_b64_tr_b16 v[52:53], v207 offset:33792
	ds_read_b64_tr_b16 v[54:55], v207 offset:34304
	s_waitcnt lgkmcnt(2)
	v_mfma_f32_32x32x16_f16 v[0:15], v[48:51], v[64:67], v[0:15]
	ds_read_b64_tr_b16 v[64:65], v207 offset:36864
	ds_read_b64_tr_b16 v[66:67], v207 offset:37376
	v_add_f32_e32 v68, v56, v68
	v_add_f32_e32 v73, v57, v68
	v_cvt_pk_f16_f32 v68, v56, v57
	v_cvt_pk_f16_f32 v69, v58, v59
	v_cvt_pk_f16_f32 v70, v60, v61
	v_cvt_pk_f16_f32 v71, v62, v63
	s_waitcnt lgkmcnt(0)
	v_mfma_f32_32x32x16_f16 v[16:31], v[48:51], v[64:67], v[16:31]
	v_add_f32_e32 v48, v58, v73
	v_add_f32_e32 v48, v59, v48
	v_add_f32_e32 v48, v60, v48
	v_add_f32_e32 v48, v61, v48
	ds_read_b64_tr_b16 v[74:75], v207 offset:37888
	ds_read_b64_tr_b16 v[76:77], v207 offset:38400
	v_add_f32_e32 v48, v62, v48
	v_add_f32_e32 v48, v63, v48
	v_mfma_f32_32x32x16_f16 v[0:15], v[68:71], v[52:55], v[0:15]
	v_add_f32_e32 v48, v32, v48
	v_add_f32_e32 v56, v33, v48
	v_cvt_pk_f16_f32 v48, v32, v33
	v_cvt_pk_f16_f32 v49, v34, v35
	v_cvt_pk_f16_f32 v50, v36, v37
	v_cvt_pk_f16_f32 v51, v38, v39
	ds_read_b64_tr_b16 v[52:53], v207 offset:34816
	ds_read_b64_tr_b16 v[54:55], v207 offset:35328
	s_waitcnt lgkmcnt(2)
	v_mfma_f32_32x32x16_f16 v[16:31], v[68:71], v[74:77], v[16:31]
	v_add_f32_e32 v32, v34, v56
	v_add_f32_e32 v56, v35, v32
	ds_read_b64_tr_b16 v[32:33], v207 offset:35840
	ds_read_b64_tr_b16 v[34:35], v207 offset:36352
	v_add_f32_e32 v36, v36, v56
	v_add_f32_e32 v36, v37, v36
	v_cvt_pk_f16_f32 v56, v40, v41
	v_cvt_pk_f16_f32 v57, v42, v43
	s_waitcnt lgkmcnt(2)
	v_mfma_f32_32x32x16_f16 v[0:15], v[48:51], v[52:55], v[0:15]
	ds_read_b64_tr_b16 v[52:53], v207 offset:38912
	ds_read_b64_tr_b16 v[54:55], v207 offset:39424
	v_cvt_pk_f16_f32 v58, v44, v45
	v_cvt_pk_f16_f32 v59, v46, v47
	ds_read_b64_tr_b16 v[60:61], v207 offset:39936
	ds_read_b64_tr_b16 v[62:63], v207 offset:40448
	v_add_f32_e32 v36, v38, v36
	v_add_f32_e32 v36, v39, v36
	v_add_f32_e32 v36, v40, v36
	s_waitcnt lgkmcnt(2)
	v_mfma_f32_32x32x16_f16 v[16:31], v[48:51], v[52:55], v[16:31]
	v_add_f32_e32 v36, v41, v36
	v_mfma_f32_32x32x16_f16 v[0:15], v[56:59], v[32:35], v[0:15]
	v_add_f32_e32 v32, v42, v36
	v_add_f32_e32 v32, v43, v32
	v_add_f32_e32 v32, v44, v32
	v_add_f32_e32 v32, v45, v32
	v_add_f32_e32 v32, v46, v32
	v_add_f32_e32 v32, v47, v32
	v_add_f32_e32 v32, v72, v32
	s_waitcnt lgkmcnt(0)
	v_mfma_f32_32x32x16_f16 v[16:31], v[56:59], v[60:63], v[16:31]
	v_mov_b32_e32 v33, v32
	s_nop 1
	v_permlane32_swap_b32_e32 v32, v33
	s_and_saveexec_b64 s[2:3], s[0:1]
	v_add_f32_e32 v32, v32, v33
	ds_write_b32 v206, v32 offset:49280
	s_or_b64 exec, exec, s[2:3]
	s_waitcnt lgkmcnt(0)
	ds_read_b128 v[32:35], v205 offset:49280
	ds_read_b128 v[36:39], v205 offset:49312
	s_lshl_b64 s[0:1], s[18:19], 10
	s_add_u32 s0, s16, s0
	s_addc_u32 s1, s17, s1
	s_waitcnt lgkmcnt(1)
	v_rcp_f32_e32 v40, v32
	v_rcp_f32_e32 v41, v33
	v_rcp_f32_e32 v42, v34
	s_lshl_b32 s2, s33, 11
	v_mul_f32_e32 v40, 0x41800000, v40
	v_mul_f32_e32 v0, v0, v40
	v_mul_f32_e32 v16, v16, v40
	v_mov_b32_e32 v40, 0
	v_cvt_pk_fp8_f32 v40, v0, v16
	v_mul_f32_e32 v16, 0x41800000, v41
	v_mul_f32_e32 v1, v1, v16
	v_mul_f32_e32 v16, v17, v16
	v_mov_b32_e32 v17, 0
	v_cvt_pk_fp8_f32 v17, v1, v16
	s_add_i32 s2, s2, 0
	v_lshlrev_b32_e32 v0, 8, v204
	v_rcp_f32_e32 v43, v35
	v_add3_u32 v0, s2, v203, v0
	v_lshrrev_b32_e32 v1, 8, v40
	s_waitcnt lgkmcnt(0)
	v_rcp_f32_e32 v44, v36
	ds_read_b128 v[32:35], v205 offset:49344
	v_rcp_f32_e32 v45, v37
	v_rcp_f32_e32 v46, v38
	v_rcp_f32_e32 v47, v39
	ds_read_b128 v[36:39], v205 offset:49376
	s_waitcnt lgkmcnt(0)
	s_barrier
	ds_write_b8 v0, v40 offset:51200
	ds_write_b8 v0, v1 offset:51232
	ds_write_b8 v0, v17 offset:51264
	v_lshrrev_b32_e32 v1, 8, v17
	ds_write_b8 v0, v1 offset:51296
	v_mul_f32_e32 v1, 0x41800000, v42
	v_mul_f32_e32 v2, v2, v1
	v_mul_f32_e32 v1, v18, v1
	v_mov_b32_e32 v16, 0
	v_cvt_pk_fp8_f32 v16, v2, v1
	v_mul_f32_e32 v1, 0x41800000, v43
	v_mul_f32_e32 v2, v3, v1
	v_mul_f32_e32 v1, v19, v1
	v_mov_b32_e32 v3, 0
	v_cvt_pk_fp8_f32 v3, v2, v1
	v_lshrrev_b32_e32 v1, 8, v16
	ds_write_b8 v0, v16 offset:51328
	ds_write_b8 v0, v1 offset:51360
	ds_write_b8 v0, v3 offset:51392
	v_lshrrev_b32_e32 v1, 8, v3
	ds_write_b8 v0, v1 offset:51424
	v_mul_f32_e32 v1, 0x41800000, v44
	v_mul_f32_e32 v2, v4, v1
	v_mul_f32_e32 v1, v20, v1
	v_mov_b32_e32 v3, 0
	v_cvt_pk_fp8_f32 v3, v2, v1
	v_mul_f32_e32 v1, 0x41800000, v45
	v_mul_f32_e32 v2, v5, v1
	v_mul_f32_e32 v1, v21, v1
	v_mov_b32_e32 v4, 0
	v_cvt_pk_fp8_f32 v4, v2, v1
	v_lshrrev_b32_e32 v1, 8, v3
	ds_write_b8 v0, v3 offset:51712
	ds_write_b8 v0, v1 offset:51744
	ds_write_b8 v0, v4 offset:51776
	v_lshrrev_b32_e32 v1, 8, v4
	ds_write_b8 v0, v1 offset:51808
	v_mul_f32_e32 v1, 0x41800000, v46
	v_mul_f32_e32 v2, v6, v1
	v_mul_f32_e32 v1, v22, v1
	v_mov_b32_e32 v3, 0
	v_cvt_pk_fp8_f32 v3, v2, v1
	v_mul_f32_e32 v1, 0x41800000, v47
	v_mul_f32_e32 v2, v7, v1
	v_mul_f32_e32 v1, v23, v1
	v_mov_b32_e32 v4, 0
	v_cvt_pk_fp8_f32 v4, v2, v1
	s_waitcnt lgkmcnt(13)
	v_rcp_f32_e32 v32, v32
	v_rcp_f32_e32 v33, v33
	v_lshrrev_b32_e32 v1, 8, v3
	ds_write_b8 v0, v3 offset:51840
	ds_write_b8 v0, v1 offset:51872
	ds_write_b8 v0, v4 offset:51904
	v_lshrrev_b32_e32 v1, 8, v4
	ds_write_b8 v0, v1 offset:51936
	v_mul_f32_e32 v1, 0x41800000, v32
	v_mul_f32_e32 v2, v8, v1
	v_mul_f32_e32 v1, v24, v1
	v_mov_b32_e32 v3, 0
	v_cvt_pk_fp8_f32 v3, v2, v1
	v_mul_f32_e32 v1, 0x41800000, v33
	v_mul_f32_e32 v2, v9, v1
	v_mul_f32_e32 v1, v25, v1
	v_mov_b32_e32 v4, 0
	v_cvt_pk_fp8_f32 v4, v2, v1
	v_rcp_f32_e32 v34, v34
	v_rcp_f32_e32 v35, v35
	v_lshrrev_b32_e32 v1, 8, v3
	ds_write_b8 v0, v3 offset:52224
	ds_write_b8 v0, v1 offset:52256
	ds_write_b8 v0, v4 offset:52288
	v_lshrrev_b32_e32 v1, 8, v4
	ds_write_b8 v0, v1 offset:52320
	v_mul_f32_e32 v1, 0x41800000, v34
	v_mul_f32_e32 v2, v10, v1
	v_mul_f32_e32 v1, v26, v1
	v_mov_b32_e32 v3, 0
	v_cvt_pk_fp8_f32 v3, v2, v1
	v_mul_f32_e32 v1, 0x41800000, v35
	v_mul_f32_e32 v2, v11, v1
	v_mul_f32_e32 v1, v27, v1
	v_mov_b32_e32 v4, 0
	v_cvt_pk_fp8_f32 v4, v2, v1
	s_waitcnt lgkmcnt(14)
	v_rcp_f32_e32 v36, v36
	v_rcp_f32_e32 v37, v37
	v_lshrrev_b32_e32 v1, 8, v3
	ds_write_b8 v0, v3 offset:52352
	ds_write_b8 v0, v1 offset:52384
	ds_write_b8 v0, v4 offset:52416
	v_lshrrev_b32_e32 v1, 8, v4
	ds_write_b8 v0, v1 offset:52448
	v_mul_f32_e32 v1, 0x41800000, v36
	v_mul_f32_e32 v2, v12, v1
	v_mul_f32_e32 v1, v28, v1
	v_mov_b32_e32 v3, 0
	v_cvt_pk_fp8_f32 v3, v2, v1
	v_mul_f32_e32 v1, 0x41800000, v37
	v_mul_f32_e32 v2, v13, v1
	v_mul_f32_e32 v1, v29, v1
	v_mov_b32_e32 v4, 0
	v_cvt_pk_fp8_f32 v4, v2, v1
	v_rcp_f32_e32 v38, v38
	v_rcp_f32_e32 v39, v39
	v_lshrrev_b32_e32 v1, 8, v3
	ds_write_b8 v0, v3 offset:52736
	ds_write_b8 v0, v1 offset:52768
	ds_write_b8 v0, v4 offset:52800
	v_lshrrev_b32_e32 v1, 8, v4
	ds_write_b8 v0, v1 offset:52832
	v_mul_f32_e32 v1, 0x41800000, v38
	v_mul_f32_e32 v2, v14, v1
	v_mul_f32_e32 v1, v30, v1
	v_mov_b32_e32 v3, 0
	v_cvt_pk_fp8_f32 v3, v2, v1
	v_mul_f32_e32 v1, 0x41800000, v39
	v_mul_f32_e32 v2, v15, v1
	v_mul_f32_e32 v1, v31, v1
	v_mov_b32_e32 v4, 0
	v_cvt_pk_fp8_f32 v4, v2, v1
	v_lshrrev_b32_e32 v1, 8, v3
	ds_write_b8 v0, v3 offset:52864
	ds_write_b8 v0, v1 offset:52896
	ds_write_b8 v0, v4 offset:52928
	v_lshrrev_b32_e32 v1, 8, v4
	ds_write_b8 v0, v1 offset:52960
	v_add_u32_e32 v4, s2, v160
	s_waitcnt lgkmcnt(0)
	v_lshl_add_u32 v0, v202, 6, v4
	v_or_b32_e32 v12, 16, v202
	ds_read_b128 v[0:3], v0 offset:51200
	v_lshl_add_u32 v4, v12, 6, v4
	s_add_u32 s0, s0, s6
	ds_read_b128 v[4:7], v4 offset:51200
	v_mov_b32_e32 v161, 0
	s_addc_u32 s1, s1, 0
	v_lshl_add_u64 v[8:9], s[0:1], 0, v[160:161]
	v_lshlrev_b32_e32 v160, 10, v202
	v_lshl_add_u64 v[10:11], v[8:9], 0, v[160:161]
	v_lshlrev_b32_e32 v160, 10, v12
	s_waitcnt lgkmcnt(1)
	global_store_dwordx4 v[10:11], v[0:3], off
	s_nop 1
	v_lshl_add_u64 v[0:1], v[8:9], 0, v[160:161]
	s_waitcnt lgkmcnt(0)
	global_store_dwordx4 v[0:1], v[4:7], off
	s_waitcnt lgkmcnt(0)
	s_barrier
	s_endpgm

	.amdhsa_kernel _Z6k_attnILi1024ELi2048ELi1024ELi1024ELi2048ELi1024ELb1ELb1EEvPKDF16_S1_S1_PKfPDF16_
		.amdhsa_group_segment_fixed_size 0
		.amdhsa_private_segment_fixed_size 0
		.amdhsa_kernarg_size 40
		.amdhsa_user_sgpr_count 2
		.amdhsa_user_sgpr_dispatch_ptr 0
		.amdhsa_user_sgpr_queue_ptr 0
		.amdhsa_user_sgpr_kernarg_segment_ptr 1
		.amdhsa_user_sgpr_dispatch_id 0
		.amdhsa_user_sgpr_kernarg_preload_length 0
		.amdhsa_user_sgpr_kernarg_preload_offset 0
		.amdhsa_user_sgpr_private_segment_size 0
		.amdhsa_uses_dynamic_stack 0
		.amdhsa_enable_private_segment 0
		.amdhsa_system_sgpr_workgroup_id_x 1
		.amdhsa_system_sgpr_workgroup_id_y 0
		.amdhsa_system_sgpr_workgroup_id_z 0
		.amdhsa_system_sgpr_workgroup_info 0
		.amdhsa_system_vgpr_workitem_id 0
		.amdhsa_next_free_vgpr 240
		.amdhsa_next_free_sgpr 66
		.amdhsa_accum_offset 240
		.amdhsa_reserve_vcc 1
		.amdhsa_float_round_mode_32 0
		.amdhsa_float_round_mode_16_64 0
		.amdhsa_float_denorm_mode_32 3
		.amdhsa_float_denorm_mode_16_64 3
		.amdhsa_dx10_clamp 1
		.amdhsa_ieee_mode 1
		.amdhsa_fp16_overflow 0
		.amdhsa_tg_split 0
		.amdhsa_exception_fp_ieee_invalid_op 0
		.amdhsa_exception_fp_denorm_src 0
		.amdhsa_exception_fp_ieee_div_zero 0
		.amdhsa_exception_fp_ieee_overflow 0
		.amdhsa_exception_fp_ieee_underflow 0
		.amdhsa_exception_fp_ieee_inexact 0
		.amdhsa_exception_int_div_zero 0
	.end_amdhsa_kernel

amdhsa.kernels:
  - .agpr_count:     0
    .args:
      - .offset:         0
        .size:           384
        .value_kind:     by_value
    .group_segment_fixed_size: 5120
    .kernarg_segment_align: 8
    .kernarg_segment_size: 384
    .language:       OpenCL C
    .language_version:
      - 2
      - 0
    .max_flat_workgroup_size: 256
    .name:           _Z6k_prep6WtArgs
    .private_segment_fixed_size: 0
    .sgpr_count:     38
    .sgpr_spill_count: 0
    .symbol:         _Z6k_prep6WtArgs.kd
    .uniform_work_group_size: 1
    .uses_dynamic_stack: false
    .vgpr_count:     29
    .vgpr_spill_count: 0
    .wavefront_size: 64
  - .agpr_count:     0
    .args:
      - .actual_access:  read_only
        .address_space:  global
        .offset:         0
        .size:           8
        .value_kind:     global_buffer
      - .actual_access:  read_only
        .address_space:  global
        .offset:         8
        .size:           8
        .value_kind:     global_buffer
      - .actual_access:  read_only
        .address_space:  global
        .offset:         16
        .size:           8
        .value_kind:     global_buffer
      - .actual_access:  write_only
        .address_space:  global
        .offset:         24
        .size:           8
        .value_kind:     global_buffer
      - .actual_access:  write_only
        .address_space:  global
        .offset:         32
        .size:           8
        .value_kind:     global_buffer
      - .actual_access:  write_only
        .address_space:  global
        .offset:         40
        .size:           8
        .value_kind:     global_buffer
      - .offset:         48
        .size:           4
        .value_kind:     by_value
    .group_segment_fixed_size: 0
    .kernarg_segment_align: 8
    .kernarg_segment_size: 52
    .language:       OpenCL C
    .language_version:
      - 2
      - 0
    .max_flat_workgroup_size: 256
    .name:           _Z4k_lnPKDF16_PKfS2_PfPDF16_Phi
    .private_segment_fixed_size: 0
    .sgpr_count:     18
    .sgpr_spill_count: 0
    .symbol:         _Z4k_lnPKDF16_PKfS2_PfPDF16_Phi.kd
    .uniform_work_group_size: 1
    .uses_dynamic_stack: false
    .vgpr_count:     59
    .vgpr_spill_count: 0
    .wavefront_size: 64
  - .agpr_count:     0
    .args:
      - .offset:         0
        .size:           56
        .value_kind:     by_value
      - .offset:         56
        .size:           72
        .value_kind:     by_value
      - .offset:         128
        .size:           176
        .value_kind:     by_value
      - .address_space:  global
        .offset:         304
        .size:           8
        .value_kind:     global_buffer
      - .offset:         312
        .size:           4
        .value_kind:     hidden_block_count_x
      - .offset:         316
        .size:           4
        .value_kind:     hidden_block_count_y
      - .offset:         320
        .size:           4
        .value_kind:     hidden_block_count_z
      - .offset:         324
        .size:           2
        .value_kind:     hidden_group_size_x
      - .offset:         326
        .size:           2
        .value_kind:     hidden_group_size_y
      - .offset:         328
        .size:           2
        .value_kind:     hidden_group_size_z
      - .offset:         330
        .size:           2
        .value_kind:     hidden_remainder_x
      - .offset:         332
        .size:           2
        .value_kind:     hidden_remainder_y
      - .offset:         334
        .size:           2
        .value_kind:     hidden_remainder_z
      - .offset:         352
        .size:           8
        .value_kind:     hidden_global_offset_x
      - .offset:         360
        .size:           8
        .value_kind:     hidden_global_offset_y
      - .offset:         368
        .size:           8
        .value_kind:     hidden_global_offset_z
      - .offset:         376
        .size:           2
        .value_kind:     hidden_grid_dims
      - .offset:         432
        .size:           4
        .value_kind:     hidden_dynamic_lds_size
    .group_segment_fixed_size: 0
    .kernarg_segment_align: 8
    .kernarg_segment_size: 568
    .language:       OpenCL C
    .language_version:
      - 2
      - 0
    .max_flat_workgroup_size: 512
    .name:           _Z6k_gemmIN3pg84EpiHILi0ELb1EEELb1EEvNS0_4GemmET_6WtTailPj
    .private_segment_fixed_size: 0
    .sgpr_count:     62
    .sgpr_spill_count: 5
    .symbol:         _Z6k_gemmIN3pg84EpiHILi0ELb1EEELb1EEvNS0_4GemmET_6WtTailPj.kd
    .uniform_work_group_size: 1
    .uses_dynamic_stack: false
    .vgpr_count:     240
    .vgpr_spill_count: 0
    .wavefront_size: 64
  - .agpr_count:     0
    .args:
      - .address_space:  global
        .offset:         0
        .size:           8
        .value_kind:     global_buffer
      - .address_space:  global
        .offset:         8
        .size:           8
        .value_kind:     global_buffer
      - .address_space:  global
        .offset:         16
        .size:           8
        .value_kind:     global_buffer
      - .address_space:  global
        .offset:         24
        .size:           8
        .value_kind:     global_buffer
      - .address_space:  global
        .offset:         32
        .size:           8
        .value_kind:     global_buffer
    .group_segment_fixed_size: 0
    .kernarg_segment_align: 8
    .kernarg_segment_size: 40
    .language:       OpenCL C
    .language_version:
      - 2
      - 0
    .max_flat_workgroup_size: 512
    .name:           _Z6k_attnILi1024ELi1024ELi1024ELi1024ELi3072ELi1024ELb1ELb1EEvPKDF16_S1_S1_PKfPDF16_
    .private_segment_fixed_size: 0
    .sgpr_count:     55
    .sgpr_spill_count: 0
    .symbol:         _Z6k_attnILi1024ELi1024ELi1024ELi1024ELi3072ELi1024ELb1ELb1EEvPKDF16_S1_S1_PKfPDF16_.kd
    .uniform_work_group_size: 1
    .uses_dynamic_stack: false
    .vgpr_count:     224
    .vgpr_spill_count: 0
    .wavefront_size: 64
  - .agpr_count:     0
    .args:
      - .address_space:  global
        .offset:         0
        .size:           8
        .value_kind:     global_buffer
      - .address_space:  global
        .offset:         8
        .size:           8
        .value_kind:     global_buffer
      - .offset:         16
        .size:           4
        .value_kind:     by_value
      - .offset:         20
        .size:           4
        .value_kind:     by_value
      - .offset:         24
        .size:           4
        .value_kind:     by_value
      - .offset:         32
        .size:           32
        .value_kind:     by_value
    .group_segment_fixed_size: 0
    .kernarg_segment_align: 8
    .kernarg_segment_size: 64
    .language:       OpenCL C
    .language_version:
      - 2
      - 0
    .max_flat_workgroup_size: 512
    .name:           _ZN2g811k_gemm128f8INS_6EpiResEEEvPKhS3_iiiT_
    .private_segment_fixed_size: 0
    .sgpr_count:     34
    .sgpr_spill_count: 0
    .symbol:         _ZN2g811k_gemm128f8INS_6EpiResEEEvPKhS3_iiiT_.kd
    .uniform_work_group_size: 1
    .uses_dynamic_stack: false
    .vgpr_count:     98
    .vgpr_spill_count: 0
    .wavefront_size: 64
  - .agpr_count:     0
    .args:
      - .address_space:  global
        .offset:         0
        .size:           8
        .value_kind:     global_buffer
      - .address_space:  global
        .offset:         8
        .size:           8
        .value_kind:     global_buffer
      - .offset:         16
        .size:           4
        .value_kind:     by_value
      - .offset:         20
        .size:           4
        .value_kind:     by_value
      - .offset:         24
        .size:           4
        .value_kind:     by_value
      - .offset:         32
        .size:           16
        .value_kind:     by_value
    .group_segment_fixed_size: 0
    .kernarg_segment_align: 8
    .kernarg_segment_size: 48
    .language:       OpenCL C
    .language_version:
      - 2
      - 0
    .max_flat_workgroup_size: 512
    .name:           _ZN2g811k_gemm128f8INS_5EpiQ8EEEvPKhS3_iiiT_
    .private_segment_fixed_size: 0
    .sgpr_count:     72
    .sgpr_spill_count: 0
    .symbol:         _ZN2g811k_gemm128f8INS_5EpiQ8EEEvPKhS3_iiiT_.kd
    .uniform_work_group_size: 1
    .uses_dynamic_stack: false
    .vgpr_count:     240
    .vgpr_spill_count: 0
    .wavefront_size: 64
  - .agpr_count:     0
    .args:
      - .address_space:  global
        .offset:         0
        .size:           8
        .value_kind:     global_buffer
      - .address_space:  global
        .offset:         8
        .size:           8
        .value_kind:     global_buffer
      - .address_space:  global
        .offset:         16
        .size:           8
        .value_kind:     global_buffer
      - .address_space:  global
        .offset:         24
        .size:           8
        .value_kind:     global_buffer
      - .address_space:  global
        .offset:         32
        .size:           8
        .value_kind:     global_buffer
    .group_segment_fixed_size: 0
    .kernarg_segment_align: 8
    .kernarg_segment_size: 40
    .language:       OpenCL C
    .language_version:
      - 2
      - 0
    .max_flat_workgroup_size: 512
    .name:           _Z6k_attnILi1024ELi2048ELi1024ELi1024ELi2048ELi1024ELb1ELb1EEvPKDF16_S1_S1_PKfPDF16_
    .private_segment_fixed_size: 0
    .sgpr_count:     52
    .sgpr_spill_count: 0
    .symbol:         _Z6k_attnILi1024ELi2048ELi1024ELi1024ELi2048ELi1024ELb1ELb1EEvPKDF16_S1_S1_PKfPDF16_.kd
    .uniform_work_group_size: 1
    .uses_dynamic_stack: false
    .vgpr_count:     224
    .vgpr_spill_count: 0
    .wavefront_size: 64
  - .agpr_count:     0
    .args:
      - .offset:         0
        .size:           56
        .value_kind:     by_value
      - .offset:         56
        .size:           72
        .value_kind:     by_value
      - .offset:         128
        .size:           176
        .value_kind:     by_value
      - .address_space:  global
        .offset:         304
        .size:           8
        .value_kind:     global_buffer
      - .offset:         312
        .size:           4
        .value_kind:     hidden_block_count_x
      - .offset:         316
        .size:           4
        .value_kind:     hidden_block_count_y
      - .offset:         320
        .size:           4
        .value_kind:     hidden_block_count_z
      - .offset:         324
        .size:           2
        .value_kind:     hidden_group_size_x
      - .offset:         326
        .size:           2
        .value_kind:     hidden_group_size_y
      - .offset:         328
        .size:           2
        .value_kind:     hidden_group_size_z
      - .offset:         330
        .size:           2
        .value_kind:     hidden_remainder_x
      - .offset:         332
        .size:           2
        .value_kind:     hidden_remainder_y
      - .offset:         334
        .size:           2
        .value_kind:     hidden_remainder_z
      - .offset:         352
        .size:           8
        .value_kind:     hidden_global_offset_x
      - .offset:         360
        .size:           8
        .value_kind:     hidden_global_offset_y
      - .offset:         368
        .size:           8
        .value_kind:     hidden_global_offset_z
      - .offset:         376
        .size:           2
        .value_kind:     hidden_grid_dims
      - .offset:         432
        .size:           4
        .value_kind:     hidden_dynamic_lds_size
    .group_segment_fixed_size: 0
    .kernarg_segment_align: 8
    .kernarg_segment_size: 568
    .language:       OpenCL C
    .language_version:
      - 2
      - 0
    .max_flat_workgroup_size: 512
    .name:           _Z6k_gemmIN3pg84EpiHILi1ELb0EEELb0EEvNS0_4GemmET_6WtTailPj
    .private_segment_fixed_size: 0
    .sgpr_count:     85
    .sgpr_spill_count: 0
    .symbol:         _Z6k_gemmIN3pg84EpiHILi1ELb0EEELb0EEvNS0_4GemmET_6WtTailPj.kd
    .uniform_work_group_size: 1
    .uses_dynamic_stack: false
    .vgpr_count:     242
    .vgpr_spill_count: 0
    .wavefront_size: 64
  - .agpr_count:     0
    .args:
      - .address_space:  global
        .offset:         0
        .size:           8
        .value_kind:     global_buffer
      - .address_space:  global
        .offset:         8
        .size:           8
        .value_kind:     global_buffer
      - .offset:         16
        .size:           4
        .value_kind:     by_value
      - .offset:         20
        .size:           4
        .value_kind:     by_value
      - .offset:         24
        .size:           4
        .value_kind:     by_value
      - .offset:         32
        .size:           32
        .value_kind:     by_value
    .group_segment_fixed_size: 0
    .kernarg_segment_align: 8
    .kernarg_segment_size: 64
    .language:       OpenCL C
    .language_version:
      - 2
      - 0
    .max_flat_workgroup_size: 512
    .name:           _ZN4g1289k_gemm128INS_8EpiRes16EEEvPKDF16_S3_iiiT_
    .private_segment_fixed_size: 0
    .sgpr_count:     35
    .sgpr_spill_count: 0
    .symbol:         _ZN4g1289k_gemm128INS_8EpiRes16EEEvPKDF16_S3_iiiT_.kd
    .uniform_work_group_size: 1
    .uses_dynamic_stack: false
    .vgpr_count:     112
    .vgpr_spill_count: 0
    .wavefront_size: 64
